# layer prologues: all weight/parameter loads issued before the first wait; icache warm chains run behind those loads
# speedup vs baseline: 1.0103x; 1.0103x over previous
_Z10k_layer_a2ILi0ELi13EEvPKDF16_PKiS3_PK15HIP_vector_typeIjLj4EES7_PKfS9_S9_S9_S9_S9_PDF16_Pf:
	s_load_dwordx2 s[8:9], s[0:1], 0x18

.Lw2b0:
	s_load_dwordx4 s[4:7], s[0:1], 0x28
	s_load_dwordx2 s[10:11], s[0:1], 0x38
	v_lshlrev_b32_e32 v2, 4, v0
	v_min_u32_e32 v1, 0x7f, v0
	v_lshlrev_b32_e32 v24, 2, v1
	v_readfirstlane_b32 s3, v0
	v_add_u32_e32 v28, 0x3400, v2
	v_add_u32_e32 v29, 0x6800, v2

.Lw2b1:
	v_add_u32_e32 v30, 0x9c00, v2
	v_add_u32_e32 v31, 0xd00, v0
	v_min_u32_e32 v31, 0xfff, v31
	v_lshlrev_b32_e32 v31, 4, v31
	s_waitcnt lgkmcnt(0)
	global_load_dwordx4 v[14:17], v2, s[8:9]
	global_load_dwordx4 v[6:9], v28, s[8:9]
	global_load_dwordx4 v[10:13], v29, s[8:9]
	global_load_dwordx4 v[18:21], v30, s[8:9]

.Lw2b2:
	global_load_dwordx4 v[32:35], v31, s[8:9]
	global_load_dword v4, v24, s[4:5]
	global_load_dword v5, v24, s[4:5] offset:512
	global_load_dword v1, v24, s[6:7]
	global_load_dword v3, v24, s[10:11]
	s_load_dword s42, s[0:1], 0x0
	s_load_dword s43, s[0:1], 0x40
	v_lshrrev_b32_e32 v48, 6, v0
	s_nop 0
	v_readfirstlane_b32 s41, v48
	s_movk_i32 s40, 0x5aa5
	s_mov_b64 exec, 0
	s_cmpk_lt_u32 s41, 6
	s_cbranch_scc1 .Lw2s0d0_13
	s_cmpk_lt_u32 s41, 9
	s_cbranch_scc1 .Lw2s0d6_13
	s_cmpk_lt_u32 s41, 11
	s_cbranch_scc1 .Lw2s0d9_13
	s_cmpk_lt_u32 s41, 12
	s_cbranch_scc1 .Lw2s0d11_13
	s_branch .Lw2t12

.Lw2e0:
	s_mov_b32 s40, 0
	s_mov_b64 exec, -1
.Lw2t3:
	s_cbranch_execz .Lw2c3
.Lw2b3:
	s_waitcnt vmcnt(8)
	ds_write_b128 v2, v[14:17]

.Lw2b4:
	s_waitcnt vmcnt(7)
	ds_write_b128 v2, v[6:9] offset:13312
	s_waitcnt vmcnt(6)
	ds_write_b128 v2, v[10:13] offset:26624
	s_waitcnt vmcnt(5)
	ds_write_b128 v2, v[18:21] offset:39936
	s_movk_i32 s4, 0x300
	v_cmp_gt_u32_e32 vcc, s4, v0
	s_waitcnt vmcnt(4)
	s_and_saveexec_b64 s[4:5], vcc
	ds_write_b128 v2, v[32:35] offset:53248

.Lw2b5:
	s_or_b64 exec, exec, s[4:5]
	s_movk_i32 s4, 0x80
	v_cmp_gt_u32_e32 vcc, s4, v0
	s_and_saveexec_b64 s[4:5], vcc
	s_cbranch_execz .LBB2_4
	s_waitcnt vmcnt(2)
	v_add_f32_e32 v2, v4, v5
	v_mov_b32_e32 v4, 0x1dd00
	v_lshl_add_u32 v4, v0, 2, v4
	s_waitcnt vmcnt(1)
	ds_write2st64_b32 v4, v2, v1 offset1:2
	s_waitcnt vmcnt(0)

.Lw2b6:
	ds_write_b32 v4, v3 offset:1024
.LBB2_4:
	s_or_b64 exec, exec, s[4:5]
	s_load_dwordx4 s[8:11], s[0:1], 0x0
	s_load_dwordx2 s[6:7], s[0:1], 0x10
	s_load_dwordx2 s[14:15], s[0:1], 0x58
	s_mov_b32 s13, 0
	v_cmp_eq_u32_e32 vcc, 0, v0
	s_and_saveexec_b64 s[4:5], vcc
	s_cbranch_execz .LBB2_6
	s_waitcnt vmcnt(1)
	v_mov_b32_e32 v1, 0

.Lw2b7:
	v_mov_b32_e32 v2, 0x1e900
	ds_write_b32 v2, v1
.LBB2_6:
	s_or_b64 exec, exec, s[4:5]
	s_waitcnt vmcnt(1)
	v_bfe_u32 v1, v0, 4, 2
	v_bfe_u32 v2, v0, 2, 2
	v_cmp_eq_u32_e32 vcc, v1, v2
	v_and_b32_e32 v2, 3, v0
	v_cmp_eq_u32_e64 s[4:5], 0, v2
	s_waitcnt vmcnt(0)

.Lw2b8:
	v_mov_b32_e32 v3, 0x3c00
	s_and_b64 s[4:5], vcc, s[4:5]
	v_cndmask_b32_e64 v4, 0, v3, s[4:5]
	v_cmp_eq_u32_e64 s[4:5], 1, v2
	s_and_b64 s[4:5], vcc, s[4:5]
	s_lshr_b32 s12, s3, 6
	v_cndmask_b32_e64 v5, 0, v3, s[4:5]
	v_cmp_eq_u32_e64 s[4:5], 2, v2
	s_and_b64 s[4:5], vcc, s[4:5]
	v_and_b32_e32 v77, 63, v0

.Lw2b9:
	v_cndmask_b32_e64 v6, 0, v3, s[4:5]
	v_cmp_eq_u32_e64 s[4:5], 3, v2
	s_and_b64 vcc, vcc, s[4:5]
	v_cndmask_b32_e32 v2, 0, v3, vcc
	v_pack_b32_f16 v73, v6, v2
	v_lshlrev_b32_e32 v2, 2, v0
	s_waitcnt lgkmcnt(0)
	s_barrier
	v_and_b32_e32 v82, 15, v0
	v_pack_b32_f16 v72, v4, v5
	s_load_dword s3, s[0:1], 0x68

.Lw2b10:
	v_and_b32_e32 v84, 0xc0, v2
	s_mul_i32 s0, s12, 0x1100
	v_and_b32_e32 v2, 48, v0
	v_bfe_u32 v5, v0, 2, 4
	v_lshlrev_b32_e32 v0, 6, v0
	s_add_i32 s4, s0, 0x10000
	v_mul_u32_u24_e32 v5, 0x110, v5
	v_and_b32_e32 v0, 0xc0, v0

.Lw2b11:
	v_mov_b32_e32 v3, 0
	s_movk_i32 s20, 0x110
	v_add3_u32 v85, s4, v5, v0
	v_mov_b32_e32 v0, s4
	v_lshlrev_b32_e32 v4, 7, v1
	v_mad_u32_u24 v5, v82, s20, v0
	v_lshlrev_b32_e32 v86, 5, v1
	v_lshlrev_b32_e32 v0, 6, v1
	v_mov_b32_e32 v1, v3
	v_lshlrev_b32_e32 v83, 4, v82
	v_lshl_add_u64 v[78:79], s[14:15], 0, v[0:1]
	v_mbcnt_lo_u32_b32 v0, -1, 0

.Lw2b12:
	v_cmp_eq_u32_e64 s[0:1], 0, v77
	v_lshl_add_u64 v[74:75], s[10:11], 0, v[2:3]
	v_or_b32_e32 v76, s4, v83
	v_or_b32_e32 v87, 28, v84
	v_or_b32_e32 v88, 32, v84
	v_or_b32_e32 v89, 36, v84
	v_or_b32_e32 v90, 40, v84
	v_or_b32_e32 v91, 44, v84
	v_or_b32_e32 v92, 48, v84
	v_or_b32_e32 v93, 52, v84
	v_or_b32_e32 v94, 56, v84
	v_or_b32_e32 v95, 60, v84

.Lw2b13:
	v_mov_b32_e32 v96, 0x1e900
	v_add_u32_e32 v97, 0x1dd00, v4
	s_mov_b32 s21, 0x1ffff00
	v_add_u32_e32 v98, v5, v2
	v_lshrrev_b32_e32 v125, 1, v86
	v_lshrrev_b32_e32 v126, 5, v86
	v_add3_u32 v125, v98, v86, v125
	v_mad_u32_u24 v126, v126, s20, v76
	v_mov_b32_e32 v99, 0x3727c5ac

.Lw2b14:
	s_mov_b32 s22, 0x800000
	v_mov_b32_e32 v100, 0xc0135761
	v_mbcnt_hi_u32_b32 v101, -1, v0
	v_mov_b32_e32 v102, 0x1dd00
	s_branch .LBB2_9
.LBB2_7:
	v_mov_b32_e32 v32, v28
	v_mov_b32_e32 v33, v24
	v_mov_b32_e32 v34, v29
	v_mov_b32_e32 v35, v25
	v_pk_add_f32 v[32:33], v[32:33], v[34:35]
.Lw2t15:
	s_cbranch_execz .Lw2c15
.Lw2b15:
	v_mov_b32_e32 v34, v30
	v_mov_b32_e32 v35, v26
	v_mov_b32_e32 v36, v31
	v_mov_b32_e32 v37, v27
	v_pk_add_f32 v[34:35], v[34:35], v[36:37]
	v_mov_b32_e32 v36, v20
	v_pk_add_f32 v[32:33], v[32:33], v[34:35]
	v_mov_b32_e32 v34, v21
	v_mov_b32_e32 v35, v22
	v_mov_b32_e32 v37, v23
	v_pk_add_f32 v[34:35], v[34:35], v[36:37]
	v_add_f32_e32 v32, 0, v32

.Lw2b16:
	v_pk_add_f32 v[34:35], v[34:35], v[34:35] op_sel:[0,1] op_sel_hi:[1,0]
	v_add_f32_e32 v32, v32, v33
	v_add_f32_e32 v36, v16, v17
	v_add_f32_e32 v38, v18, v19
	v_mov_b32_e32 v33, v12
	v_mov_b32_e32 v35, v13
	v_mov_b32_e32 v37, v14
	v_mov_b32_e32 v39, v15
	v_pk_add_f32 v[32:33], v[32:33], v[34:35]
	v_pk_add_f32 v[34:35], v[36:37], v[38:39]
	v_mov_b32_e32 v36, v8
	v_pk_add_f32 v[32:33], v[32:33], v[34:35]

.Lw2b17:
	v_mov_b32_e32 v34, v9
	v_mov_b32_e32 v35, v10
	v_mov_b32_e32 v37, v11
	v_pk_add_f32 v[34:35], v[34:35], v[36:37]
	v_pk_add_f32 v[32:33], v[32:33], v[32:33] op_sel:[0,1] op_sel_hi:[1,0]
	v_pk_add_f32 v[34:35], v[34:35], v[34:35] op_sel:[0,1] op_sel_hi:[1,0]
	v_add_f32_e32 v36, v4, v5
	v_add_f32_e32 v38, v6, v7
	v_mov_b32_e32 v33, v0
	v_mov_b32_e32 v35, v1
	v_mov_b32_e32 v37, v2

.Lw2b18:
	v_mov_b32_e32 v39, v3
	v_pk_add_f32 v[32:33], v[32:33], v[34:35]
	v_pk_add_f32 v[34:35], v[36:37], v[38:39]
	s_nop 0
	v_pk_add_f32 v[32:33], v[32:33], v[34:35]
	v_and_b32_e32 v34, 64, v101
	v_add_f32_e32 v32, v32, v33
	v_xor_b32_e32 v33, 16, v101
	v_add_u32_e32 v34, 64, v34
	v_cmp_lt_i32_e32 vcc, v33, v34
	s_nop 1
	v_cndmask_b32_e32 v33, v101, v33, vcc

.Lw2b19:
	v_lshlrev_b32_e32 v42, 2, v33
	ds_bpermute_b32 v33, v42, v32
	s_waitcnt lgkmcnt(0)
	v_add_f32_e32 v32, v32, v33
	v_xor_b32_e32 v33, 32, v101
	v_cmp_lt_i32_e32 vcc, v33, v34
	s_nop 1
	v_cndmask_b32_e32 v33, v101, v33, vcc
	v_lshlrev_b32_e32 v43, 2, v33
	ds_bpermute_b32 v33, v43, v32
	s_waitcnt lgkmcnt(0)
	v_add_f32_e32 v44, v32, v33
	v_fmamk_f32 v29, v44, 0xbc000000, v29

.Lw2b20:
	v_fmamk_f32 v25, v44, 0xbc000000, v25
	v_fmamk_f32 v41, v44, 0xbc000000, v31
	v_fmamk_f32 v40, v44, 0xbc000000, v30
	v_fmac_f32_e32 v28, 0xbc000000, v44
	v_fmamk_f32 v39, v44, 0xbc000000, v27
	v_fmac_f32_e32 v24, 0xbc000000, v44
	v_mov_b32_e32 v30, v29
	v_mov_b32_e32 v31, v25

.Lw2b21:
	v_fmamk_f32 v38, v44, 0xbc000000, v26
	v_mov_b32_e32 v26, v28
	v_mov_b32_e32 v27, v24
	v_pk_mul_f32 v[30:31], v[30:31], v[30:31]
	v_mov_b32_e32 v32, v41
	v_mov_b32_e32 v33, v39
	v_pk_fma_f32 v[26:27], v[26:27], v[26:27], v[30:31]
	v_mov_b32_e32 v30, v40
	v_mov_b32_e32 v31, v38
	v_pk_mul_f32 v[32:33], v[32:33], v[32:33]
	v_fmamk_f32 v37, v44, 0xbc000000, v21

.Lw2b22:
	v_pk_fma_f32 v[30:31], v[30:31], v[30:31], v[32:33]
	v_fmamk_f32 v36, v44, 0xbc000000, v20
	v_fmamk_f32 v23, v44, 0xbc000000, v23
	v_fmac_f32_e32 v22, 0xbc000000, v44
	v_pk_add_f32 v[26:27], v[26:27], v[30:31]
	v_pk_mul_f32 v[20:21], v[22:23], v[22:23]
	v_pk_mul_f32 v[30:31], v[36:37], v[36:37]

.Lw2b23:
	v_fmac_f32_e32 v12, 0xbc000000, v44
	v_pk_mov_b32 v[32:33], v[30:31], v[20:21] op_sel:[1,0]
	v_mov_b32_e32 v31, v21
	v_pk_add_f32 v[20:21], v[32:33], v[30:31]
	v_fmamk_f32 v34, v44, 0xbc000000, v18
	v_fmamk_f32 v31, v44, 0xbc000000, v15
	v_fmamk_f32 v30, v44, 0xbc000000, v14
	v_fmamk_f32 v13, v44, 0xbc000000, v13

.Lw2b24:
	v_mul_f32_e32 v18, v12, v12
	v_pk_add_f32 v[14:15], v[26:27], v[26:27] op_sel:[0,1] op_sel_hi:[1,0]
	v_fmamk_f32 v35, v44, 0xbc000000, v19
	v_mul_f32_e32 v32, v13, v13
	v_mov_b32_e32 v15, v18
	v_pk_add_f32 v[18:19], v[20:21], v[20:21] op_sel:[0,1] op_sel_hi:[1,0]
	v_fmamk_f32 v17, v44, 0xbc000000, v17
	v_mov_b32_e32 v19, v32
	v_fmac_f32_e32 v16, 0xbc000000, v44
	v_pk_add_f32 v[14:15], v[14:15], v[18:19]

.Lw2b25:
	v_mul_f32_e32 v18, v17, v17
	v_mul_f32_e32 v20, v35, v35
	v_mul_f32_e32 v33, v30, v30
	v_mul_f32_e32 v45, v31, v31
	v_pk_fma_f32 v[18:19], v[16:17], v[16:17], v[18:19] op_sel_hi:[1,1,0]
	v_pk_fma_f32 v[20:21], v[34:35], v[34:35], v[20:21] op_sel_hi:[1,1,0]
	v_mov_b32_e32 v19, v33
	v_mov_b32_e32 v21, v45
	v_pk_add_f32 v[18:19], v[18:19], v[20:21]
	v_fmamk_f32 v33, v44, 0xbc000000, v9

.Lw2b26:
	v_fmamk_f32 v32, v44, 0xbc000000, v8
	v_fmamk_f32 v11, v44, 0xbc000000, v11
	v_fmac_f32_e32 v10, 0xbc000000, v44
	v_pk_add_f32 v[14:15], v[14:15], v[18:19]
	v_pk_mul_f32 v[8:9], v[10:11], v[10:11]
	v_pk_mul_f32 v[18:19], v[32:33], v[32:33]
	v_fmamk_f32 v1, v44, 0xbc000000, v1
	v_pk_mov_b32 v[20:21], v[18:19], v[8:9] op_sel:[1,0]

.Lw2b27:
	v_mov_b32_e32 v19, v9
	v_pk_add_f32 v[8:9], v[20:21], v[18:19]
	v_fmac_f32_e32 v0, 0xbc000000, v44
	v_fmamk_f32 v19, v44, 0xbc000000, v7
	v_fmamk_f32 v18, v44, 0xbc000000, v6
	v_mul_f32_e32 v20, v0, v0
	v_mul_f32_e32 v21, v1, v1
	v_pk_add_f32 v[6:7], v[14:15], v[14:15] op_sel:[0,1] op_sel_hi:[1,0]
	v_pk_add_f32 v[8:9], v[8:9], v[8:9] op_sel:[0,1] op_sel_hi:[1,0]

.Lw2b28:
	v_fmamk_f32 v5, v44, 0xbc000000, v5
	v_mov_b32_e32 v7, v20
	v_mov_b32_e32 v9, v21
	v_fmac_f32_e32 v4, 0xbc000000, v44
	v_fmamk_f32 v3, v44, 0xbc000000, v3
	v_fmamk_f32 v2, v44, 0xbc000000, v2
	v_pk_add_f32 v[6:7], v[6:7], v[8:9]
	v_mul_f32_e32 v8, v5, v5
	v_mul_f32_e32 v14, v19, v19

.Lw2b29:
	v_mul_f32_e32 v26, v2, v2
	v_mul_f32_e32 v27, v3, v3
	v_pk_fma_f32 v[8:9], v[4:5], v[4:5], v[8:9] op_sel_hi:[1,1,0]
	v_pk_fma_f32 v[14:15], v[18:19], v[18:19], v[14:15] op_sel_hi:[1,1,0]
	v_mov_b32_e32 v9, v26
	v_mov_b32_e32 v15, v27
	v_pk_add_f32 v[8:9], v[8:9], v[14:15]
	s_nop 0
	v_pk_add_f32 v[6:7], v[6:7], v[8:9]
	s_nop 0
	v_add_f32_e32 v6, v6, v7

.Lw2b30:
	ds_bpermute_b32 v7, v42, v6
	s_waitcnt lgkmcnt(0)
	v_add_f32_e32 v6, v6, v7
	ds_bpermute_b32 v7, v43, v6
	s_waitcnt lgkmcnt(0)
	v_add_f32_e32 v6, v6, v7
	v_fmamk_f32 v6, v6, 0x3c000000, v99
	v_mul_f32_e32 v7, 0x4b800000, v6
	v_cmp_gt_f32_e32 vcc, s22, v6
	s_nop 1
	v_cndmask_b32_e32 v6, v6, v7, vcc

.Lw2b31:
	v_rsq_f32_e32 v14, v6
	ds_read_b128 v[6:9], v97 offset:512
	ds_read_b128 v[42:45], v97 offset:528
	ds_read_b128 v[46:49], v97 offset:1024
	ds_read_b128 v[50:53], v97 offset:1040
	v_mul_f32_e32 v15, 0x45800000, v14
	v_cndmask_b32_e32 v20, v14, v15, vcc
	v_pk_mul_f32 v[26:27], v[20:21], v[28:29] op_sel_hi:[0,1]
	s_waitcnt lgkmcnt(1)

.Lw2b32:
	v_pk_fma_f32 v[6:7], v[6:7], v[26:27], v[46:47]
	v_or_b32_e32 v14, s4, v82
	v_pk_mul_f32 v[26:27], v[6:7], v[6:7]
	v_ashrrev_i32_e32 v15, 31, v14
	v_fmamk_f32 v21, v26, 0xbdd2d3e8, v100
	v_mul_f32_e32 v21, v6, v21
	v_fmamk_f32 v26, v27, 0xbdd2d3e8, v100
	v_exp_f32_e32 v21, v21
	v_mul_f32_e32 v26, v7, v26
	v_exp_f32_e32 v26, v26
	v_lshlrev_b64 v[14:15], 8, v[14:15]

.Lw2b33:
	v_add_f32_e32 v21, 1.0, v21
	v_rcp_f32_e32 v28, v21
	v_add_f32_e32 v21, 1.0, v26
	v_pk_mul_f32 v[26:27], v[20:21], v[40:41] op_sel_hi:[0,1]
	v_pk_fma_f32 v[8:9], v[8:9], v[26:27], v[48:49]
	v_rcp_f32_e32 v29, v21
	v_pk_mul_f32 v[40:41], v[8:9], v[8:9]
	v_mad_u32_u24 v104, v86, 6, v83
	s_lshl_b32 s12, s4, 8
	v_mov_b32_e32 v105, 0

.Lw2b34:
	v_add_u32_e32 v104, s12, v104
	s_nop 0
	v_lshl_add_u64 v[104:105], v[78:79], 0, v[104:105]
	v_fmamk_f32 v21, v40, 0xbdd2d3e8, v100
	v_mul_f32_e32 v21, v8, v21
	v_exp_f32_e32 v21, v21
	v_fmamk_f32 v14, v41, 0xbdd2d3e8, v100
	v_pk_mul_f32 v[6:7], v[6:7], v[28:29]
	v_mul_f32_e32 v14, v9, v14
	v_cvt_pk_f16_f32 v6, v6, v7

.Lw2b35:
	v_add_f32_e32 v7, 1.0, v21
	v_exp_f32_e32 v21, v14
	v_rcp_f32_e32 v28, v7
	v_pk_mul_f32 v[14:15], v[20:21], v[24:25] op_sel_hi:[0,1]
	s_waitcnt lgkmcnt(0)
	v_pk_fma_f32 v[14:15], v[42:43], v[14:15], v[50:51]
	v_add_f32_e32 v7, 1.0, v21
	v_pk_mul_f32 v[24:25], v[14:15], v[14:15]
	v_rcp_f32_e32 v29, v7
	v_fmamk_f32 v24, v24, 0xbdd2d3e8, v100
	v_mul_f32_e32 v24, v14, v24

.Lw2b36:
	v_exp_f32_e32 v24, v24
	v_fmamk_f32 v21, v25, 0xbdd2d3e8, v100
	v_mul_f32_e32 v21, v15, v21
	v_pk_mul_f32 v[8:9], v[8:9], v[28:29]
	v_add_f32_e32 v7, 1.0, v24
	v_pk_mul_f32 v[24:25], v[20:21], v[38:39] op_sel_hi:[0,1]
	v_pk_fma_f32 v[24:25], v[44:45], v[24:25], v[52:53]
	v_exp_f32_e32 v21, v21
	v_pk_mul_f32 v[38:39], v[24:25], v[24:25]
	v_rcp_f32_e32 v40, v7

.Lw2b37:
	v_fmamk_f32 v38, v38, 0xbdd2d3e8, v100
	v_fmamk_f32 v39, v39, 0xbdd2d3e8, v100
	v_mul_f32_e32 v38, v24, v38
	v_mul_f32_e32 v39, v25, v39
	v_exp_f32_e32 v38, v38
	v_exp_f32_e32 v39, v39
	v_add_f32_e32 v7, 1.0, v21
	v_mov_b32_e32 v21, v86
	v_add_f32_e32 v38, 1.0, v38
	v_add_f32_e32 v39, 1.0, v39
	v_rcp_f32_e32 v38, v38
	v_rcp_f32_e32 v39, v39
	v_rcp_f32_e32 v41, v7

.Lw2b38:
	v_pk_mul_f32 v[24:25], v[24:25], v[38:39]
	s_nop 0
	s_nop 0
	v_lshl_add_u32 v7, v21, 2, v102
	v_add_u32_e32 v54, 0x420, v7
	v_add_u32_e32 v48, 0x428, v7
	v_add_u32_e32 v52, 0x430, v7
	ds_read2_b32 v[38:39], v7 offset0:138 offset1:139
	ds_read2_b32 v[42:43], v7 offset0:142 offset1:143

.Lw2b39:
	ds_read2_b32 v[44:45], v7 offset0:140 offset1:141
	ds_read2_b32 v[46:47], v7 offset0:136 offset1:137
	v_add_u32_e32 v7, 0x438, v7
	ds_read2_b32 v[48:49], v48 offset1:1
	ds_read2_b32 v[50:51], v7 offset1:1
	ds_read2_b32 v[52:53], v52 offset1:1
	ds_read2_b32 v[54:55], v54 offset1:1

.Lw2b40:
	v_cvt_pk_f16_f32 v7, v8, v9
	v_pk_mul_f32 v[8:9], v[14:15], v[40:41]
	s_nop 0
	v_cvt_pk_f16_f32 v8, v8, v9
	v_pk_mul_f32 v[14:15], v[20:21], v[36:37] op_sel_hi:[0,1]
	s_waitcnt lgkmcnt(0)
	v_pk_fma_f32 v[14:15], v[46:47], v[14:15], v[54:55]
	v_pk_mul_f32 v[22:23], v[20:21], v[22:23] op_sel_hi:[0,1]
	v_pk_mul_f32 v[28:29], v[14:15], v[14:15]

.Lw2b41:
	v_pk_fma_f32 v[22:23], v[38:39], v[22:23], v[48:49]
	v_fmamk_f32 v9, v28, 0xbdd2d3e8, v100
	v_mul_f32_e32 v9, v14, v9
	v_fmamk_f32 v28, v29, 0xbdd2d3e8, v100
	v_exp_f32_e32 v9, v9
	v_mul_f32_e32 v28, v15, v28
	v_exp_f32_e32 v29, v28
	v_pk_mul_f32 v[36:37], v[22:23], v[22:23]
	v_add_f32_e32 v9, 1.0, v9
	v_rcp_f32_e32 v28, v9

.Lw2b42:
	v_add_f32_e32 v9, 1.0, v29
	v_rcp_f32_e32 v29, v9
	v_fmamk_f32 v9, v36, 0xbdd2d3e8, v100
	v_mul_f32_e32 v9, v22, v9
	v_exp_f32_e32 v36, v9
	v_cvt_pk_f16_f32 v9, v24, v25
	v_fmamk_f32 v24, v37, 0xbdd2d3e8, v100
	v_pk_mul_f32 v[16:17], v[20:21], v[16:17] op_sel_hi:[0,1]
	v_mul_f32_e32 v24, v23, v24
	v_pk_fma_f32 v[16:17], v[44:45], v[16:17], v[52:53]

.Lw2b43:
	v_pk_mul_f32 v[14:15], v[14:15], v[28:29]
	v_exp_f32_e32 v29, v24
	v_pk_mul_f32 v[24:25], v[16:17], v[16:17]
	v_cvt_pk_f16_f32 v14, v14, v15
	v_fmamk_f32 v24, v24, 0xbdd2d3e8, v100
	v_mul_f32_e32 v24, v16, v24
	v_exp_f32_e32 v24, v24
	v_add_f32_e32 v15, 1.0, v36
	v_rcp_f32_e32 v28, v15
	v_add_f32_e32 v15, 1.0, v29
	v_rcp_f32_e32 v29, v15

.Lw2b44:
	v_add_f32_e32 v15, 1.0, v24
	v_fmamk_f32 v24, v25, 0xbdd2d3e8, v100
	v_mul_f32_e32 v36, v17, v24
	v_pk_mul_f32 v[24:25], v[20:21], v[34:35] op_sel_hi:[0,1]
	v_pk_fma_f32 v[24:25], v[42:43], v[24:25], v[50:51]
	v_exp_f32_e32 v37, v36
	v_pk_mul_f32 v[34:35], v[24:25], v[24:25]
	v_rcp_f32_e32 v36, v15
	v_fmamk_f32 v34, v34, 0xbdd2d3e8, v100
	v_fmamk_f32 v35, v35, 0xbdd2d3e8, v100

.Lw2b45:
	v_mul_f32_e32 v34, v24, v34
	v_mul_f32_e32 v35, v25, v35
	v_exp_f32_e32 v34, v34
	v_exp_f32_e32 v35, v35
	v_add_f32_e32 v15, 1.0, v37
	v_rcp_f32_e32 v37, v15
	v_add_f32_e32 v34, 1.0, v34
	v_add_f32_e32 v35, 1.0, v35
	v_rcp_f32_e32 v34, v34
	v_rcp_f32_e32 v35, v35
	v_pk_mul_f32 v[22:23], v[22:23], v[28:29]
	v_pk_mul_f32 v[16:17], v[16:17], v[36:37]

.Lw2b46:
	v_pk_mul_f32 v[24:25], v[24:25], v[34:35]
	s_nop 0
	v_cvt_pk_f16_f32 v16, v16, v17
	v_lshl_add_u32 v15, v21, 2, v102
	v_add_u32_e32 v50, 0x440, v15
	v_add_u32_e32 v44, 0x448, v15
	v_add_u32_e32 v48, 0x450, v15
	ds_read2_b32 v[34:35], v15 offset0:146 offset1:147

.Lw2b47:
	ds_read2_b32 v[38:39], v15 offset0:150 offset1:151
	ds_read2_b32 v[40:41], v15 offset0:148 offset1:149
	ds_read2_b32 v[42:43], v15 offset0:144 offset1:145
	v_add_u32_e32 v15, 0x458, v15
	ds_read2_b32 v[44:45], v44 offset1:1
	ds_read2_b32 v[46:47], v15 offset1:1
	ds_read2_b32 v[48:49], v48 offset1:1
	ds_read2_b32 v[50:51], v50 offset1:1

.Lw2b48:
	v_cvt_pk_f16_f32 v15, v22, v23
	v_pk_mul_f32 v[12:13], v[20:21], v[12:13] op_sel_hi:[0,1]
	s_waitcnt lgkmcnt(0)
	v_pk_fma_f32 v[12:13], v[42:43], v[12:13], v[50:51]
	v_pk_mul_f32 v[28:29], v[20:21], v[30:31] op_sel_hi:[0,1]
	v_pk_mul_f32 v[22:23], v[12:13], v[12:13]
	v_pk_fma_f32 v[28:29], v[34:35], v[28:29], v[44:45]
	v_fmamk_f32 v17, v22, 0xbdd2d3e8, v100

.Lw2b49:
	v_mul_f32_e32 v17, v12, v17
	v_fmamk_f32 v22, v23, 0xbdd2d3e8, v100
	v_exp_f32_e32 v17, v17
	v_mul_f32_e32 v22, v13, v22
	v_exp_f32_e32 v23, v22
	v_pk_mul_f32 v[30:31], v[28:29], v[28:29]
	v_add_f32_e32 v17, 1.0, v17
	v_rcp_f32_e32 v22, v17
	v_add_f32_e32 v17, 1.0, v23
	v_rcp_f32_e32 v23, v17
	v_fmamk_f32 v17, v30, 0xbdd2d3e8, v100

.Lw2b50:
	v_mul_f32_e32 v17, v28, v17
	v_exp_f32_e32 v30, v17
	v_pk_mul_f32 v[12:13], v[12:13], v[22:23]
	v_cvt_pk_f16_f32 v17, v24, v25
	v_cvt_pk_f16_f32 v22, v12, v13
	v_fmamk_f32 v12, v31, 0xbdd2d3e8, v100
	v_mul_f32_e32 v12, v29, v12
	v_exp_f32_e32 v31, v12
	v_pk_mul_f32 v[12:13], v[20:21], v[32:33] op_sel_hi:[0,1]
	v_pk_fma_f32 v[12:13], v[40:41], v[12:13], v[48:49]

.Lw2b51:
	v_add_f32_e32 v23, 1.0, v30
	v_pk_mul_f32 v[24:25], v[12:13], v[12:13]
	v_rcp_f32_e32 v30, v23
	v_fmamk_f32 v24, v24, 0xbdd2d3e8, v100
	v_mul_f32_e32 v24, v12, v24
	v_exp_f32_e32 v24, v24
	v_add_f32_e32 v23, 1.0, v31
	v_pk_mul_f32 v[10:11], v[20:21], v[10:11] op_sel_hi:[0,1]
	v_rcp_f32_e32 v31, v23
	v_add_f32_e32 v23, 1.0, v24
	v_fmamk_f32 v24, v25, 0xbdd2d3e8, v100

.Lw2b52:
	v_pk_fma_f32 v[10:11], v[38:39], v[10:11], v[46:47]
	v_mul_f32_e32 v32, v13, v24
	v_pk_mul_f32 v[24:25], v[10:11], v[10:11]
	v_exp_f32_e32 v33, v32
	v_fmamk_f32 v24, v24, 0xbdd2d3e8, v100
	v_fmamk_f32 v25, v25, 0xbdd2d3e8, v100
	v_mul_f32_e32 v24, v10, v24
	v_mul_f32_e32 v25, v11, v25
	v_exp_f32_e32 v24, v24
	v_exp_f32_e32 v25, v25

.Lw2b53:
	v_rcp_f32_e32 v32, v23
	v_add_f32_e32 v23, 1.0, v33
	v_add_f32_e32 v24, 1.0, v24
	v_add_f32_e32 v25, 1.0, v25
	v_rcp_f32_e32 v24, v24
	v_rcp_f32_e32 v25, v25
	v_rcp_f32_e32 v33, v23
	v_pk_mul_f32 v[10:11], v[10:11], v[24:25]
	s_nop 0
	v_pk_mul_f32 v[12:13], v[12:13], v[32:33]
	v_lshl_add_u32 v21, v21, 2, v102
	v_add_u32_e32 v24, 0x468, v21

.Lw2b54:
	ds_read2_b32 v[34:35], v21 offset0:154 offset1:155
	ds_read2_b32 v[36:37], v21 offset0:158 offset1:159
	ds_read2_b32 v[38:39], v21 offset0:156 offset1:157
	ds_read2_b32 v[40:41], v21 offset0:152 offset1:153
	v_add_u32_e32 v23, 0x460, v21
	v_add_u32_e32 v25, 0x470, v21
	v_add_u32_e32 v21, 0x478, v21

.Lw2b55:
	ds_read2_b32 v[42:43], v24 offset1:1
	ds_read2_b32 v[44:45], v21 offset1:1
	ds_read2_b32 v[46:47], v25 offset1:1
	ds_read2_b32 v[48:49], v23 offset1:1
	v_pk_mul_f32 v[24:25], v[28:29], v[30:31]
	s_nop 0
	v_cvt_pk_f16_f32 v23, v24, v25
	v_cvt_pk_f16_f32 v24, v12, v13

.Lw2b56:
	v_pk_mul_f32 v[4:5], v[20:21], v[4:5] op_sel_hi:[0,1]
	s_waitcnt lgkmcnt(0)
	v_pk_fma_f32 v[4:5], v[40:41], v[4:5], v[48:49]
	ds_write_b128 v125, v[6:9]
	v_pk_mul_f32 v[12:13], v[4:5], v[4:5]
	v_pk_mul_f32 v[0:1], v[20:21], v[0:1] op_sel_hi:[0,1]
	v_fmamk_f32 v12, v12, 0xbdd2d3e8, v100
	v_fmamk_f32 v13, v13, 0xbdd2d3e8, v100

.Lw2b57:
	v_mul_f32_e32 v12, v4, v12
	v_mul_f32_e32 v13, v5, v13
	v_exp_f32_e32 v12, v12
	v_exp_f32_e32 v13, v13
	v_pk_fma_f32 v[0:1], v[38:39], v[0:1], v[46:47]
	v_cvt_pk_f16_f32 v25, v10, v11
	v_add_f32_e32 v6, 1.0, v12
	v_add_f32_e32 v7, 1.0, v13
	v_rcp_f32_e32 v6, v6
	v_rcp_f32_e32 v7, v7
	v_pk_mul_f32 v[10:11], v[0:1], v[0:1]
	v_pk_mul_f32 v[2:3], v[20:21], v[2:3] op_sel_hi:[0,1]

.Lw2b58:
	v_pk_fma_f32 v[2:3], v[36:37], v[2:3], v[44:45]
	v_pk_mul_f32 v[4:5], v[4:5], v[6:7]
	v_pk_mul_f32 v[6:7], v[20:21], v[18:19] op_sel_hi:[0,1]
	v_pk_fma_f32 v[6:7], v[34:35], v[6:7], v[42:43]
	v_cvt_pk_f16_f32 v4, v4, v5
	v_pk_mul_f32 v[8:9], v[6:7], v[6:7]
	s_mov_b64 s[4:5], 0
	v_fmamk_f32 v8, v8, 0xbdd2d3e8, v100

.Lw2b59:
	v_mul_f32_e32 v8, v6, v8
	v_fmamk_f32 v9, v9, 0xbdd2d3e8, v100
	v_exp_f32_e32 v8, v8
	v_mul_f32_e32 v9, v7, v9
	v_exp_f32_e32 v9, v9
	ds_write_b128 v125, v[14:17] offset:16
	v_add_f32_e32 v5, 1.0, v8
	v_rcp_f32_e32 v8, v5
	v_add_f32_e32 v5, 1.0, v9
	v_rcp_f32_e32 v9, v5
	v_fmamk_f32 v5, v10, 0xbdd2d3e8, v100

.Lw2b60:
	v_mul_f32_e32 v5, v0, v5
	v_fmamk_f32 v10, v11, 0xbdd2d3e8, v100
	v_exp_f32_e32 v5, v5
	v_mul_f32_e32 v10, v1, v10
	v_exp_f32_e32 v10, v10
	v_pk_mul_f32 v[6:7], v[6:7], v[8:9]
	v_add_f32_e32 v5, 1.0, v5
	v_rcp_f32_e32 v8, v5
	v_add_f32_e32 v5, 1.0, v10
	v_pk_mul_f32 v[10:11], v[2:3], v[2:3]
	ds_write_b128 v125, v[22:25] offset:32

.Lw2b61:
	v_fmamk_f32 v9, v10, 0xbdd2d3e8, v100
	v_mul_f32_e32 v9, v2, v9
	v_exp_f32_e32 v10, v9
	v_fmamk_f32 v9, v11, 0xbdd2d3e8, v100
	v_mul_f32_e32 v9, v3, v9
	v_exp_f32_e32 v11, v9
	v_rcp_f32_e32 v9, v5
	v_add_f32_e32 v5, 1.0, v10
	v_rcp_f32_e32 v10, v5
	v_add_f32_e32 v5, 1.0, v11
	v_rcp_f32_e32 v11, v5
	v_pk_mul_f32 v[0:1], v[0:1], v[8:9]

.Lw2b62:
	v_cvt_pk_f16_f32 v5, v6, v7
	v_cvt_pk_f16_f32 v6, v0, v1
	v_pk_mul_f32 v[0:1], v[2:3], v[10:11]
	s_nop 0
	v_cvt_pk_f16_f32 v7, v0, v1
	ds_write_b128 v125, v[4:7] offset:48
	ds_read_b128 v[4:7], v126
	ds_read_b128 v[8:11], v126 offset:1088

.Lw2b63:
	ds_read_b128 v[12:15], v126 offset:2176
	ds_read_b128 v[16:19], v126 offset:3264
	s_waitcnt lgkmcnt(3)
	global_store_dwordx4 v[104:105], v[4:7], off
	s_waitcnt lgkmcnt(2)
	global_store_dwordx4 v[104:105], v[8:11], off offset:1024
	s_waitcnt lgkmcnt(1)
	global_store_dwordx4 v[104:105], v[12:15], off offset:2048
	s_waitcnt lgkmcnt(0)
	global_store_dwordx4 v[104:105], v[16:19], off offset:3072
.LBB2_8:
.Lw2t64:
	s_cbranch_execz .Lw2c64
.Lw2b64:
	s_and_b64 vcc, exec, s[4:5]
	s_cbranch_vccnz .LBB2_92
.LBB2_9:
	v_mov_b32_e32 v0, 0
	s_and_saveexec_b64 s[4:5], s[0:1]
	s_cbranch_execz .LBB2_13
	s_mov_b64 s[14:15], exec
	v_mbcnt_lo_u32_b32 v0, s14, 0
	v_mbcnt_hi_u32_b32 v0, s15, v0
	v_cmp_eq_u32_e32 vcc, 0, v0
	s_and_saveexec_b64 s[10:11], vcc
	s_bcnt1_i32_b64 s12, s[14:15]
	v_mov_b32_e32 v1, s12

.Lw2b65:
	ds_add_rtn_u32 v1, v96, v1
	s_or_b64 exec, exec, s[10:11]
	s_waitcnt lgkmcnt(0)
	v_readfirstlane_b32 s10, v1
	s_nop 1
	v_add_u32_e32 v0, s10, v0

.Lw2b66:
	ds_read_b128 v[28:31], v97
	ds_read_b128 v[24:27], v97 offset:16
	ds_read_b128 v[20:23], v97 offset:32
	ds_read_b128 v[16:19], v97 offset:48
	ds_read_b128 v[12:15], v97 offset:64
	ds_read_b128 v[8:11], v97 offset:80
	ds_read_b128 v[4:7], v97 offset:96
	ds_read_b128 v[0:3], v97 offset:112

.Lw2b67:
	s_lshl_b32 s4, s10, 4
	s_ashr_i32 s5, s4, 31
	v_lshl_add_u64 v[80:81], s[4:5], 2, v[74:75]
	s_mov_b32 s5, 0
	s_mov_b64 s[18:19], -1
	s_branch .LBB2_16
.LBB2_15:
	s_or_b64 exec, exec, s[14:15]
	v_mov_b32_e32 v48, v77
	ds_read_b128 v[32:35], v98
	ds_read_b128 v[36:39], v98 offset:64
	ds_read_b128 v[40:43], v98 offset:128
.Lw2t68:
	s_cbranch_execz .Lw2c68
.Lw2b68:
	ds_read_b128 v[44:47], v98 offset:192
	s_nop 0
	v_lshlrev_b32_e32 v48, 4, v48
	v_lshl_add_u32 v103, s5, 15, v48
	ds_read_b128 v[48:51], v103
	ds_read_b128 v[52:55], v103 offset:1024
	ds_read_b128 v[56:59], v103 offset:2048
	ds_read_b128 v[60:63], v103 offset:3072

.Lw2b69:
	ds_read_b128 v[64:67], v103 offset:4096
	ds_read_b128 v[68:71], v103 offset:5120
	ds_read_b128 v[104:107], v103 offset:6144
	ds_read_b128 v[108:111], v103 offset:7168
	s_waitcnt lgkmcnt(7)
	v_mfma_f32_16x16x32_f16 v[28:31], v[48:51], v[32:35], v[28:31]
	s_waitcnt lgkmcnt(6)
	v_mfma_f32_16x16x32_f16 v[24:27], v[52:55], v[32:35], v[24:27]
	s_waitcnt lgkmcnt(5)

.Lw2b70:
	v_mfma_f32_16x16x32_f16 v[20:23], v[56:59], v[32:35], v[20:23]
	s_waitcnt lgkmcnt(4)
	v_mfma_f32_16x16x32_f16 v[16:19], v[60:63], v[32:35], v[16:19]
	ds_read_b128 v[48:51], v103 offset:8192
	ds_read_b128 v[52:55], v103 offset:9216
	ds_read_b128 v[56:59], v103 offset:10240
	ds_read_b128 v[60:63], v103 offset:11264
	s_waitcnt lgkmcnt(7)
	v_mfma_f32_16x16x32_f16 v[12:15], v[64:67], v[32:35], v[12:15]

.Lw2b71:
	s_waitcnt lgkmcnt(6)
	v_mfma_f32_16x16x32_f16 v[8:11], v[68:71], v[32:35], v[8:11]
	s_waitcnt lgkmcnt(5)
	v_mfma_f32_16x16x32_f16 v[4:7], v[104:107], v[32:35], v[4:7]
	s_waitcnt lgkmcnt(4)
	v_mfma_f32_16x16x32_f16 v[0:3], v[108:111], v[32:35], v[0:3]
	ds_read_b128 v[32:35], v103 offset:12288
	ds_read_b128 v[64:67], v103 offset:13312
	ds_read_b128 v[68:71], v103 offset:14336

.Lw2b72:
	ds_read_b128 v[104:107], v103 offset:15360
	s_waitcnt lgkmcnt(7)
	v_mfma_f32_16x16x32_f16 v[28:31], v[48:51], v[36:39], v[28:31]
	s_waitcnt lgkmcnt(6)
	v_mfma_f32_16x16x32_f16 v[24:27], v[52:55], v[36:39], v[24:27]
	s_waitcnt lgkmcnt(5)
	v_mfma_f32_16x16x32_f16 v[20:23], v[56:59], v[36:39], v[20:23]
	s_waitcnt lgkmcnt(4)
	v_mfma_f32_16x16x32_f16 v[16:19], v[60:63], v[36:39], v[16:19]

.Lw2b73:
	ds_read_b128 v[48:51], v103 offset:16384
	ds_read_b128 v[52:55], v103 offset:17408
	ds_read_b128 v[56:59], v103 offset:18432
	ds_read_b128 v[60:63], v103 offset:19456
	s_waitcnt lgkmcnt(7)
	v_mfma_f32_16x16x32_f16 v[12:15], v[32:35], v[36:39], v[12:15]
	s_waitcnt lgkmcnt(6)
	v_mfma_f32_16x16x32_f16 v[8:11], v[64:67], v[36:39], v[8:11]
	s_waitcnt lgkmcnt(5)

.Lw2b74:
	v_mfma_f32_16x16x32_f16 v[4:7], v[68:71], v[36:39], v[4:7]
	s_waitcnt lgkmcnt(4)
	v_mfma_f32_16x16x32_f16 v[0:3], v[104:107], v[36:39], v[0:3]
	ds_read_b128 v[32:35], v103 offset:20480
	ds_read_b128 v[36:39], v103 offset:21504
	ds_read_b128 v[64:67], v103 offset:22528
	ds_read_b128 v[68:71], v103 offset:23552
	s_waitcnt lgkmcnt(7)
	v_mfma_f32_16x16x32_f16 v[28:31], v[48:51], v[40:43], v[28:31]

.Lw2b75:
	s_waitcnt lgkmcnt(6)
	v_mfma_f32_16x16x32_f16 v[24:27], v[52:55], v[40:43], v[24:27]
	s_waitcnt lgkmcnt(5)
	v_mfma_f32_16x16x32_f16 v[20:23], v[56:59], v[40:43], v[20:23]
	s_waitcnt lgkmcnt(4)
	v_mfma_f32_16x16x32_f16 v[16:19], v[60:63], v[40:43], v[16:19]
	ds_read_b128 v[48:51], v103 offset:24576
	ds_read_b128 v[52:55], v103 offset:25600
	ds_read_b128 v[56:59], v103 offset:26624

.Lw2b76:
	ds_read_b128 v[60:63], v103 offset:27648
	s_waitcnt lgkmcnt(7)
	v_mfma_f32_16x16x32_f16 v[12:15], v[32:35], v[40:43], v[12:15]
	s_waitcnt lgkmcnt(6)
	v_mfma_f32_16x16x32_f16 v[8:11], v[36:39], v[40:43], v[8:11]
	s_waitcnt lgkmcnt(5)
	v_mfma_f32_16x16x32_f16 v[4:7], v[64:67], v[40:43], v[4:7]
	s_waitcnt lgkmcnt(4)
	v_mfma_f32_16x16x32_f16 v[0:3], v[68:71], v[40:43], v[0:3]

.Lw2b77:
	ds_read_b128 v[32:35], v103 offset:28672
	ds_read_b128 v[36:39], v103 offset:29696
	ds_read_b128 v[40:43], v103 offset:30720
	ds_read_b128 v[64:67], v103 offset:31744
	s_waitcnt lgkmcnt(7)
	v_mfma_f32_16x16x32_f16 v[28:31], v[48:51], v[44:47], v[28:31]
	s_waitcnt lgkmcnt(6)
	v_mfma_f32_16x16x32_f16 v[24:27], v[52:55], v[44:47], v[24:27]
	s_waitcnt lgkmcnt(5)

.Lw2b78:
	v_mfma_f32_16x16x32_f16 v[20:23], v[56:59], v[44:47], v[20:23]
	s_waitcnt lgkmcnt(4)
	v_mfma_f32_16x16x32_f16 v[16:19], v[60:63], v[44:47], v[16:19]
	s_waitcnt lgkmcnt(3)
	v_mfma_f32_16x16x32_f16 v[12:15], v[32:35], v[44:47], v[12:15]
	s_waitcnt lgkmcnt(2)
	v_mfma_f32_16x16x32_f16 v[8:11], v[36:39], v[44:47], v[8:11]
	s_waitcnt lgkmcnt(1)
	v_mfma_f32_16x16x32_f16 v[4:7], v[40:43], v[44:47], v[4:7]
	s_waitcnt lgkmcnt(0)

.Lw2b79:
	v_mfma_f32_16x16x32_f16 v[0:3], v[64:67], v[44:47], v[0:3]
	s_mov_b32 s5, 1
	s_mov_b64 s[18:19], 0
	s_and_b64 vcc, exec, s[10:11]
	s_cbranch_vccnz .LBB2_7
.LBB2_16:
	s_mul_i32 s12, s5, 0x186a1
	v_lshl_add_u64 v[32:33], s[12:13], 2, v[80:81]
	global_load_dword v113, v[32:33], off
	global_load_dword v103, v[32:33], off offset:16
	s_mov_b32 s14, s13

.Lw2b80:
	s_mov_b32 s15, s13
	s_mul_i32 s12, s5, 0xc3500
	s_lshl_b64 s[10:11], s[12:13], 2
	s_mov_b32 s12, s13
	v_mov_b64_e32 v[34:35], s[14:15]
	v_mov_b64_e32 v[32:33], s[12:13]
	s_add_u32 s16, s6, s10
	ds_write_b128 v85, v[32:35]
	ds_write_b128 v85, v[32:35] offset:16
	ds_write_b128 v85, v[32:35] offset:32
	ds_write_b128 v85, v[32:35] offset:48
	s_addc_u32 s17, s7, s11

.Lw2b81:
	v_mov_b32_e32 v116, 0x3f86a0
	s_waitcnt vmcnt(1)
	v_add_u32_e32 v32, v113, v82
	s_waitcnt vmcnt(0)
	v_cmp_lt_i32_e32 vcc, v32, v103
	s_and_saveexec_b64 s[10:11], vcc
	s_cbranch_execz .LBB2_18
	v_ashrrev_i32_e32 v33, 31, v32
	v_lshl_add_u64 v[32:33], v[32:33], 2, s[16:17]
	global_load_dword v116, v[32:33], off

.LBB2_19:
	s_waitcnt vmcnt(0)
	v_mov_b32_e32 v116, v114
	s_cbranch_execnz .LBB2_90
.LBB2_20:
.Lw2t83:
	s_cbranch_execz .Lw2c83
.Lw2b83:
	s_nop 2
	v_mov_b32_e32 v104, v63
	v_mov_b32_e32 v106, v62
	v_mov_b32_e32 v105, v61
	v_mov_b32_e32 v108, v60
	v_mov_b32_e32 v109, v59
	v_mov_b32_e32 v111, v58
	v_mov_b32_e32 v110, v57
	v_mov_b32_e32 v112, v56
	v_mov_b32_e32 v107, v115
	v_cmp_lt_i32_e32 vcc, v113, v103
	s_cbranch_vccz .LBB2_19
	v_or_b32_e32 v32, 4, v84
	s_waitcnt vmcnt(0)
	ds_bpermute_b32 v66, v84, v116

.Lw2b84:
	ds_bpermute_b32 v123, v32, v116
	v_or_b32_e32 v32, 8, v84
	v_or_b32_e32 v34, 12, v84
	ds_bpermute_b32 v122, v32, v116
	ds_bpermute_b32 v121, v34, v116
	v_or_b32_e32 v34, 16, v84
	ds_bpermute_b32 v120, v34, v116
	v_or_b32_e32 v34, 20, v84
	ds_bpermute_b32 v119, v34, v116

.Lw2b85:
	s_waitcnt lgkmcnt(5)
	v_lshlrev_b32_e32 v32, 8, v66
	s_waitcnt lgkmcnt(4)
	v_lshlrev_b32_e32 v33, 8, v123
	v_or_b32_e32 v34, 24, v84
	v_and_or_b32 v32, v32, s21, v83
	v_and_or_b32 v33, v33, s21, v83
	ds_bpermute_b32 v118, v34, v116
	ds_bpermute_b32 v117, v87, v116
	global_load_dwordx4 v[60:63], v32, s[8:9]

.Lw2b86:
	global_load_dwordx4 v[56:59], v33, s[8:9]
	s_waitcnt lgkmcnt(5)
	v_lshlrev_b32_e32 v32, 8, v122
	s_waitcnt lgkmcnt(4)
	v_lshlrev_b32_e32 v33, 8, v121
	v_and_or_b32 v32, v32, s21, v83
	v_and_or_b32 v33, v33, s21, v83
	global_load_dwordx4 v[52:55], v32, s[8:9]
	global_load_dwordx4 v[48:51], v33, s[8:9]
	s_waitcnt lgkmcnt(3)

.Lw2b87:
	v_lshlrev_b32_e32 v32, 8, v120
	s_waitcnt lgkmcnt(2)
	v_lshlrev_b32_e32 v33, 8, v119
	v_and_or_b32 v32, v32, s21, v83
	v_and_or_b32 v33, v33, s21, v83
	global_load_dwordx4 v[44:47], v32, s[8:9]
	global_load_dwordx4 v[40:43], v33, s[8:9]
	s_waitcnt lgkmcnt(1)
	v_lshlrev_b32_e32 v32, 8, v118
	s_waitcnt lgkmcnt(0)
	v_lshlrev_b32_e32 v33, 8, v117

.Lw2b88:
	v_and_or_b32 v32, v32, s21, v83
	v_and_or_b32 v33, v33, s21, v83
	global_load_dwordx4 v[36:39], v32, s[8:9]
	s_nop 0
	global_load_dwordx4 v[32:35], v33, s[8:9]
	v_or_b32_e32 v64, 16, v82
	v_add_u32_e32 v64, v64, v113
	v_cmp_lt_i32_e32 vcc, v64, v103
	v_mov_b32_e32 v114, 0x3f86a0
	s_and_saveexec_b64 s[14:15], vcc

.Lw2b89:
	s_cbranch_execz .LBB2_23
	v_ashrrev_i32_e32 v65, 31, v64
	v_lshl_add_u64 v[64:65], v[64:65], 2, s[16:17]
	global_load_dword v114, v[64:65], off
.LBB2_23:
	s_or_b64 exec, exec, s[14:15]
	v_ashrrev_i32_e32 v124, 17, v66
	v_cmp_ne_u32_e32 vcc, v124, v107
	s_cmp_lg_u64 vcc, 0
	s_cselect_b64 s[14:15], -1, 0
	s_and_b64 s[18:19], s[14:15], vcc
	v_mov_b32_e32 v115, v107
	v_mov_b32_e32 v68, v112
	v_mov_b32_e32 v69, v110

.Lw2b90:
	v_mov_b32_e32 v70, v111
	v_mov_b32_e32 v71, v109
	v_mov_b32_e32 v64, v108
	v_mov_b32_e32 v65, v105
	v_mov_b32_e32 v66, v106
	v_mov_b32_e32 v67, v104
	s_and_saveexec_b64 s[14:15], s[18:19]
	s_cbranch_execz .LBB2_27
	v_cmp_gt_i32_e32 vcc, 16, v107
	s_and_saveexec_b64 s[18:19], vcc
	s_cbranch_execz .LBB2_26
	v_cvt_pk_f16_f32 v67, v111, v109
	v_cvt_pk_f16_f32 v66, v112, v110

.Lw2b91:
	v_cvt_pk_f16_f32 v65, v106, v104
	v_cvt_pk_f16_f32 v64, v108, v105
	v_mad_u64_u32 v[68:69], s[24:25], v107, s20, v[76:77]
	ds_write_b128 v68, v[64:67]
.LBB2_26:
	s_or_b64 exec, exec, s[18:19]
	v_mov_b32_e32 v68, 0
	v_mov_b32_e32 v115, v124
	v_mov_b32_e32 v69, v68
	v_mov_b32_e32 v70, v68
	v_mov_b32_e32 v71, v68
	v_mov_b32_e32 v64, v68
.Lw2t92:
	s_cbranch_execz .Lw2c92
.Lw2b92:
	v_mov_b32_e32 v65, v68
	v_mov_b32_e32 v66, v68
	v_mov_b32_e32 v67, v68
.LBB2_27:
	s_or_b64 exec, exec, s[14:15]
	v_ashrrev_i32_e32 v123, 17, v123
	s_waitcnt vmcnt(7)
	v_mfma_f32_16x16x16_f16 v[64:67], v[72:73], v[60:61], v[64:67]
	v_cmp_ne_u32_e32 vcc, v123, v115
	s_cmp_lg_u64 vcc, 0
	s_cselect_b64 s[14:15], -1, 0
	v_mfma_f32_16x16x16_f16 v[60:63], v[72:73], v[62:63], v[68:71]
	s_and_b64 s[18:19], s[14:15], vcc
	s_and_saveexec_b64 s[14:15], s[18:19]

.Lw2b93:
	s_cbranch_execz .LBB2_31
	v_cmp_gt_i32_e32 vcc, 16, v115
	s_and_saveexec_b64 s[18:19], vcc
	s_cbranch_execz .LBB2_30
	s_nop 1
	v_cvt_pk_f16_f32 v63, v62, v63
	v_cvt_pk_f16_f32 v62, v60, v61
	v_cvt_pk_f16_f32 v61, v66, v67
	v_cvt_pk_f16_f32 v60, v64, v65
	v_mad_u64_u32 v[64:65], s[24:25], v115, s20, v[76:77]

.Lw2b94:
	ds_write_b128 v64, v[60:63]

.LBB2_31:
	s_or_b64 exec, exec, s[14:15]
	v_ashrrev_i32_e32 v68, 17, v122
.Lw2t95:
	s_cbranch_execz .Lw2c95
.Lw2b95:
	s_waitcnt vmcnt(6)
	v_mfma_f32_16x16x16_f16 v[64:67], v[72:73], v[56:57], v[64:67]
	v_cmp_ne_u32_e32 vcc, v68, v115
	s_cmp_lg_u64 vcc, 0
	s_cselect_b64 s[14:15], -1, 0
	v_mfma_f32_16x16x16_f16 v[56:59], v[72:73], v[58:59], v[60:63]
	s_and_b64 s[18:19], s[14:15], vcc
	s_and_saveexec_b64 s[14:15], s[18:19]
	s_cbranch_execz .LBB2_35
	v_cmp_gt_i32_e32 vcc, 16, v115
	s_and_saveexec_b64 s[18:19], vcc
	s_cbranch_execz .LBB2_34
	s_nop 1

.Lw2b96:
	v_cvt_pk_f16_f32 v59, v58, v59
	v_cvt_pk_f16_f32 v58, v56, v57
	v_cvt_pk_f16_f32 v57, v66, v67
	v_cvt_pk_f16_f32 v56, v64, v65
	v_mad_u64_u32 v[60:61], s[24:25], v115, s20, v[76:77]
	ds_write_b128 v60, v[56:59]
.LBB2_34:
	s_or_b64 exec, exec, s[18:19]
	s_nop 0
	v_mov_b32_e32 v56, 0
.Lw2t97:
	s_cbranch_execz .Lw2c97
.Lw2b97:
	v_mov_b32_e32 v115, v68
	v_mov_b32_e32 v57, v56
	v_mov_b32_e32 v58, v56
	v_mov_b32_e32 v59, v56
	v_mov_b32_e32 v64, v56
	v_mov_b32_e32 v65, v56
	v_mov_b32_e32 v66, v56
	v_mov_b32_e32 v67, v56
.LBB2_35:
	s_or_b64 exec, exec, s[14:15]
	v_ashrrev_i32_e32 v68, 17, v121
	s_waitcnt vmcnt(5)
	v_mfma_f32_16x16x16_f16 v[60:63], v[72:73], v[52:53], v[64:67]
	v_cmp_ne_u32_e32 vcc, v68, v115
	s_cmp_lg_u64 vcc, 0
	s_cselect_b64 s[14:15], -1, 0
.Lw2t98:
	s_cbranch_execz .Lw2c98
.Lw2b98:
	v_mfma_f32_16x16x16_f16 v[52:55], v[72:73], v[54:55], v[56:59]
	s_and_b64 s[18:19], s[14:15], vcc
	s_and_saveexec_b64 s[14:15], s[18:19]
	s_cbranch_execz .LBB2_39
	v_cmp_gt_i32_e32 vcc, 16, v115
	s_and_saveexec_b64 s[18:19], vcc
	s_cbranch_execz .LBB2_38
	s_nop 1
	v_cvt_pk_f16_f32 v55, v54, v55
	v_cvt_pk_f16_f32 v54, v52, v53
	v_cvt_pk_f16_f32 v53, v62, v63

.Lw2b99:
	v_cvt_pk_f16_f32 v52, v60, v61
	v_mad_u64_u32 v[56:57], s[24:25], v115, s20, v[76:77]
	ds_write_b128 v56, v[52:55]
.LBB2_38:
	s_or_b64 exec, exec, s[18:19]
	s_nop 0
	v_mov_b32_e32 v52, 0
	v_mov_b32_e32 v115, v68
	v_mov_b32_e32 v53, v52
	v_mov_b32_e32 v54, v52
	v_mov_b32_e32 v55, v52
	v_mov_b32_e32 v60, v52

.Lw2b100:
	v_mov_b32_e32 v61, v52
	v_mov_b32_e32 v62, v52
	v_mov_b32_e32 v63, v52
.LBB2_39:
	s_or_b64 exec, exec, s[14:15]
	v_ashrrev_i32_e32 v64, 17, v120
	s_waitcnt vmcnt(4)
	v_mfma_f32_16x16x16_f16 v[56:59], v[72:73], v[48:49], v[60:63]
	v_cmp_ne_u32_e32 vcc, v64, v115
	s_cmp_lg_u64 vcc, 0
	s_cselect_b64 s[14:15], -1, 0
	v_mfma_f32_16x16x16_f16 v[48:51], v[72:73], v[50:51], v[52:55]
	s_and_b64 s[18:19], s[14:15], vcc
	s_and_saveexec_b64 s[14:15], s[18:19]

.Lw2b101:
	s_cbranch_execz .LBB2_43
	v_cmp_gt_i32_e32 vcc, 16, v115
	s_and_saveexec_b64 s[18:19], vcc
	s_cbranch_execz .LBB2_42
	s_nop 1
	v_cvt_pk_f16_f32 v51, v50, v51
	v_cvt_pk_f16_f32 v50, v48, v49
	v_cvt_pk_f16_f32 v49, v58, v59
	v_cvt_pk_f16_f32 v48, v56, v57
	v_mad_u64_u32 v[52:53], s[24:25], v115, s20, v[76:77]

.Lw2b102:
	ds_write_b128 v52, v[48:51]

.LBB2_43:
	s_or_b64 exec, exec, s[14:15]
	v_ashrrev_i32_e32 v60, 17, v119
.Lw2t103:
	s_cbranch_execz .Lw2c103
.Lw2b103:
	s_waitcnt vmcnt(3)
	v_mfma_f32_16x16x16_f16 v[52:55], v[72:73], v[44:45], v[56:59]
	v_cmp_ne_u32_e32 vcc, v60, v115
	s_cmp_lg_u64 vcc, 0
	s_cselect_b64 s[14:15], -1, 0
	v_mfma_f32_16x16x16_f16 v[44:47], v[72:73], v[46:47], v[48:51]
	s_and_b64 s[18:19], s[14:15], vcc
	s_and_saveexec_b64 s[14:15], s[18:19]
	s_cbranch_execz .LBB2_47
	v_cmp_gt_i32_e32 vcc, 16, v115
	s_and_saveexec_b64 s[18:19], vcc
	s_cbranch_execz .LBB2_46
	s_nop 1

.Lw2b104:
	v_cvt_pk_f16_f32 v47, v46, v47
	v_cvt_pk_f16_f32 v46, v44, v45
	v_cvt_pk_f16_f32 v45, v54, v55
	v_cvt_pk_f16_f32 v44, v52, v53
	v_mad_u64_u32 v[48:49], s[24:25], v115, s20, v[76:77]
	ds_write_b128 v48, v[44:47]
.LBB2_46:
	s_or_b64 exec, exec, s[18:19]
	s_nop 0
	v_mov_b32_e32 v44, 0
.Lw2t105:
	s_cbranch_execz .Lw2c105
.Lw2b105:
	v_mov_b32_e32 v115, v60
	v_mov_b32_e32 v45, v44
	v_mov_b32_e32 v46, v44
	v_mov_b32_e32 v47, v44
	v_mov_b32_e32 v52, v44
	v_mov_b32_e32 v53, v44
	v_mov_b32_e32 v54, v44
	v_mov_b32_e32 v55, v44
.LBB2_47:
	s_or_b64 exec, exec, s[14:15]
	v_ashrrev_i32_e32 v56, 17, v118
	s_waitcnt vmcnt(2)
	v_mfma_f32_16x16x16_f16 v[48:51], v[72:73], v[40:41], v[52:55]
	v_cmp_ne_u32_e32 vcc, v56, v115
	s_cmp_lg_u64 vcc, 0
	s_cselect_b64 s[14:15], -1, 0
.Lw2t106:
	s_cbranch_execz .Lw2c106
.Lw2b106:
	v_mfma_f32_16x16x16_f16 v[40:43], v[72:73], v[42:43], v[44:47]
	s_and_b64 s[18:19], s[14:15], vcc
	s_and_saveexec_b64 s[14:15], s[18:19]
	s_cbranch_execz .LBB2_51
	v_cmp_gt_i32_e32 vcc, 16, v115
	s_and_saveexec_b64 s[18:19], vcc
	s_cbranch_execz .LBB2_50
	s_nop 1
	v_cvt_pk_f16_f32 v43, v42, v43
	v_cvt_pk_f16_f32 v42, v40, v41
	v_cvt_pk_f16_f32 v41, v50, v51

.Lw2b107:
	v_cvt_pk_f16_f32 v40, v48, v49
	v_mad_u64_u32 v[44:45], s[24:25], v115, s20, v[76:77]
	ds_write_b128 v44, v[40:43]
.LBB2_50:
	s_or_b64 exec, exec, s[18:19]
	s_nop 0
	v_mov_b32_e32 v40, 0
	v_mov_b32_e32 v115, v56
	v_mov_b32_e32 v41, v40
	v_mov_b32_e32 v42, v40
	v_mov_b32_e32 v43, v40
	v_mov_b32_e32 v48, v40

.Lw2b108:
	v_mov_b32_e32 v49, v40
	v_mov_b32_e32 v50, v40
	v_mov_b32_e32 v51, v40
.LBB2_51:
	s_or_b64 exec, exec, s[14:15]
	v_ashrrev_i32_e32 v52, 17, v117
	s_waitcnt vmcnt(1)
	v_mfma_f32_16x16x16_f16 v[44:47], v[72:73], v[36:37], v[48:51]
	v_cmp_ne_u32_e32 vcc, v52, v115
	s_cmp_lg_u64 vcc, 0
	s_cselect_b64 s[14:15], -1, 0
	v_mfma_f32_16x16x16_f16 v[36:39], v[72:73], v[38:39], v[40:43]
	s_and_b64 s[18:19], s[14:15], vcc
	s_and_saveexec_b64 s[14:15], s[18:19]

.Lw2b109:
	s_cbranch_execz .LBB2_55
	v_cmp_gt_i32_e32 vcc, 16, v115
	s_and_saveexec_b64 s[18:19], vcc
	s_cbranch_execz .LBB2_54
	s_nop 1
	v_cvt_pk_f16_f32 v39, v38, v39
	v_cvt_pk_f16_f32 v38, v36, v37
	v_cvt_pk_f16_f32 v37, v46, v47
	v_cvt_pk_f16_f32 v36, v44, v45
	v_mad_u64_u32 v[40:41], s[24:25], v115, s20, v[76:77]

.Lw2b110:
	ds_write_b128 v40, v[36:39]

.LBB2_55:
	s_or_b64 exec, exec, s[14:15]
	s_waitcnt vmcnt(0)
.Lw2t111:
	s_cbranch_execz .Lw2c111
.Lw2b111:
	v_mfma_f32_16x16x16_f16 v[60:63], v[72:73], v[32:33], v[44:47]
	v_add_u32_e32 v32, 8, v113
	v_cmp_lt_i32_e32 vcc, v32, v103
	v_mfma_f32_16x16x16_f16 v[56:59], v[72:73], v[34:35], v[36:39]
	s_cbranch_vccz .LBB2_89
	ds_bpermute_b32 v123, v88, v116
	ds_bpermute_b32 v122, v89, v116
	ds_bpermute_b32 v121, v90, v116
	ds_bpermute_b32 v120, v91, v116

.Lw2b112:
	ds_bpermute_b32 v119, v92, v116
	ds_bpermute_b32 v118, v93, v116
	s_waitcnt lgkmcnt(5)
	v_lshlrev_b32_e32 v32, 8, v123
	s_waitcnt lgkmcnt(4)
	v_lshlrev_b32_e32 v33, 8, v122
	v_and_or_b32 v32, v32, s21, v83
	v_and_or_b32 v33, v33, s21, v83
	ds_bpermute_b32 v117, v94, v116
	ds_bpermute_b32 v116, v95, v116

.Lw2b113:
	global_load_dwordx4 v[68:71], v32, s[8:9]
	global_load_dwordx4 v[64:67], v33, s[8:9]
	s_waitcnt lgkmcnt(5)
	v_lshlrev_b32_e32 v32, 8, v121
	s_waitcnt lgkmcnt(4)
	v_lshlrev_b32_e32 v33, 8, v120
	v_and_or_b32 v32, v32, s21, v83
	v_and_or_b32 v33, v33, s21, v83
	global_load_dwordx4 v[52:55], v32, s[8:9]

.Lw2b114:
	global_load_dwordx4 v[48:51], v33, s[8:9]
	s_waitcnt lgkmcnt(3)
	v_lshlrev_b32_e32 v32, 8, v119
	s_waitcnt lgkmcnt(2)
	v_lshlrev_b32_e32 v33, 8, v118
	v_and_or_b32 v32, v32, s21, v83
	v_and_or_b32 v33, v33, s21, v83
	global_load_dwordx4 v[44:47], v32, s[8:9]
	global_load_dwordx4 v[40:43], v33, s[8:9]
	s_waitcnt lgkmcnt(1)

.Lw2b115:
	v_lshlrev_b32_e32 v32, 8, v117
	s_waitcnt lgkmcnt(0)
	v_lshlrev_b32_e32 v33, 8, v116
	v_and_or_b32 v32, v32, s21, v83
	v_and_or_b32 v33, v33, s21, v83
	global_load_dwordx4 v[36:39], v32, s[8:9]
	s_nop 0
	global_load_dwordx4 v[32:35], v33, s[8:9]
	v_ashrrev_i32_e32 v123, 17, v123
	v_cmp_ne_u32_e32 vcc, v123, v115
	s_cmp_lg_u64 vcc, 0
	s_cselect_b64 s[14:15], -1, 0

.Lw2b116:
	s_and_b64 s[18:19], s[14:15], vcc
	s_and_saveexec_b64 s[14:15], s[18:19]
	s_cbranch_execz .LBB2_60
	v_cmp_gt_i32_e32 vcc, 16, v115
	s_and_saveexec_b64 s[18:19], vcc
	s_cbranch_execz .LBB2_59
	v_cvt_pk_f16_f32 v59, v58, v59
	v_cvt_pk_f16_f32 v58, v56, v57
	v_cvt_pk_f16_f32 v57, v62, v63
	v_cvt_pk_f16_f32 v56, v60, v61

.LBB2_60:
	s_or_b64 exec, exec, s[14:15]
.Lw2t118:
	s_cbranch_execz .Lw2c118
.Lw2b118:
	v_ashrrev_i32_e32 v122, 17, v122
	s_waitcnt vmcnt(7)
	v_mfma_f32_16x16x16_f16 v[60:63], v[72:73], v[68:69], v[60:63]
	v_cmp_ne_u32_e32 vcc, v122, v115
	s_cmp_lg_u64 vcc, 0
	s_cselect_b64 s[14:15], -1, 0
	v_mfma_f32_16x16x16_f16 v[56:59], v[72:73], v[70:71], v[56:59]
	s_and_b64 s[18:19], s[14:15], vcc
	s_and_saveexec_b64 s[14:15], s[18:19]
	s_cbranch_execz .LBB2_64
	v_cmp_gt_i32_e32 vcc, 16, v115
	s_and_saveexec_b64 s[18:19], vcc
	s_cbranch_execz .LBB2_63

.Lw2b119:
	s_nop 1
	v_cvt_pk_f16_f32 v59, v58, v59
	v_cvt_pk_f16_f32 v58, v56, v57
	v_cvt_pk_f16_f32 v57, v62, v63
	v_cvt_pk_f16_f32 v56, v60, v61
	v_mad_u64_u32 v[60:61], s[24:25], v115, s20, v[76:77]
	ds_write_b128 v60, v[56:59]
.LBB2_63:
	s_or_b64 exec, exec, s[18:19]
	s_nop 0
.Lw2t120:
	s_cbranch_execz .Lw2c120
.Lw2b120:
	v_mov_b32_e32 v56, 0
	v_mov_b32_e32 v115, v122
	v_mov_b32_e32 v57, v56
	v_mov_b32_e32 v58, v56
	v_mov_b32_e32 v59, v56
	v_mov_b32_e32 v60, v56
	v_mov_b32_e32 v61, v56
	v_mov_b32_e32 v62, v56
	v_mov_b32_e32 v63, v56
.LBB2_64:
	s_or_b64 exec, exec, s[14:15]
	v_ashrrev_i32_e32 v68, 17, v121
	s_waitcnt vmcnt(6)
	v_mfma_f32_16x16x16_f16 v[60:63], v[72:73], v[64:65], v[60:63]
	v_cmp_ne_u32_e32 vcc, v68, v115
.Lw2t121:
	s_cbranch_execz .Lw2c121
.Lw2b121:
	s_cmp_lg_u64 vcc, 0
	s_cselect_b64 s[14:15], -1, 0
	v_mfma_f32_16x16x16_f16 v[56:59], v[72:73], v[66:67], v[56:59]
	s_and_b64 s[18:19], s[14:15], vcc
	s_and_saveexec_b64 s[14:15], s[18:19]
	s_cbranch_execz .LBB2_68
	v_cmp_gt_i32_e32 vcc, 16, v115
	s_and_saveexec_b64 s[18:19], vcc
	s_cbranch_execz .LBB2_67
	s_nop 1
	v_cvt_pk_f16_f32 v59, v58, v59
	v_cvt_pk_f16_f32 v58, v56, v57

.Lw2b122:
	v_cvt_pk_f16_f32 v57, v62, v63
	v_cvt_pk_f16_f32 v56, v60, v61
	v_mad_u64_u32 v[60:61], s[24:25], v115, s20, v[76:77]
	ds_write_b128 v60, v[56:59]
.LBB2_67:
	s_or_b64 exec, exec, s[18:19]
	s_nop 0
	v_mov_b32_e32 v56, 0
	v_mov_b32_e32 v115, v68
	v_mov_b32_e32 v57, v56
	v_mov_b32_e32 v58, v56
	v_mov_b32_e32 v59, v56
.Lw2t123:
	s_cbranch_execz .Lw2c123
.Lw2b123:
	v_mov_b32_e32 v60, v56
	v_mov_b32_e32 v61, v56
	v_mov_b32_e32 v62, v56
	v_mov_b32_e32 v63, v56
.LBB2_68:
	s_or_b64 exec, exec, s[14:15]
	v_ashrrev_i32_e32 v64, 17, v120
	s_waitcnt vmcnt(5)
	v_mfma_f32_16x16x16_f16 v[60:63], v[72:73], v[52:53], v[60:63]
	v_cmp_ne_u32_e32 vcc, v64, v115
	s_cmp_lg_u64 vcc, 0
	s_cselect_b64 s[14:15], -1, 0
	v_mfma_f32_16x16x16_f16 v[52:55], v[72:73], v[54:55], v[56:59]
	s_and_b64 s[18:19], s[14:15], vcc

.Lw2b124:
	s_and_saveexec_b64 s[14:15], s[18:19]
	s_cbranch_execz .LBB2_72
	v_cmp_gt_i32_e32 vcc, 16, v115
	s_and_saveexec_b64 s[18:19], vcc
	s_cbranch_execz .LBB2_71
	s_nop 1
	v_cvt_pk_f16_f32 v55, v54, v55
	v_cvt_pk_f16_f32 v54, v52, v53
	v_cvt_pk_f16_f32 v53, v62, v63
	v_cvt_pk_f16_f32 v52, v60, v61
	v_mad_u64_u32 v[56:57], s[24:25], v115, s20, v[76:77]

.Lw2b125:
	ds_write_b128 v56, v[52:55]

.LBB2_72:
	s_or_b64 exec, exec, s[14:15]
.Lw2t126:
	s_cbranch_execz .Lw2c126
.Lw2b126:
	v_ashrrev_i32_e32 v64, 17, v119
	s_waitcnt vmcnt(4)
	v_mfma_f32_16x16x16_f16 v[56:59], v[72:73], v[48:49], v[60:63]
	v_cmp_ne_u32_e32 vcc, v64, v115
	s_cmp_lg_u64 vcc, 0
	s_cselect_b64 s[14:15], -1, 0
	v_mfma_f32_16x16x16_f16 v[48:51], v[72:73], v[50:51], v[52:55]
	s_and_b64 s[18:19], s[14:15], vcc
	s_and_saveexec_b64 s[14:15], s[18:19]
	s_cbranch_execz .LBB2_76
	v_cmp_gt_i32_e32 vcc, 16, v115
	s_and_saveexec_b64 s[18:19], vcc
	s_cbranch_execz .LBB2_75

.Lw2b127:
	s_nop 1
	v_cvt_pk_f16_f32 v51, v50, v51
	v_cvt_pk_f16_f32 v50, v48, v49
	v_cvt_pk_f16_f32 v49, v58, v59
	v_cvt_pk_f16_f32 v48, v56, v57
	v_mad_u64_u32 v[52:53], s[24:25], v115, s20, v[76:77]
	ds_write_b128 v52, v[48:51]
.LBB2_75:
	s_or_b64 exec, exec, s[18:19]
	s_nop 0
.Lw2t128:
	s_cbranch_execz .Lw2c128
.Lw2b128:
	v_mov_b32_e32 v48, 0
	v_mov_b32_e32 v115, v64
	v_mov_b32_e32 v49, v48
	v_mov_b32_e32 v50, v48
	v_mov_b32_e32 v51, v48
	v_mov_b32_e32 v56, v48
	v_mov_b32_e32 v57, v48
	v_mov_b32_e32 v58, v48
	v_mov_b32_e32 v59, v48
.LBB2_76:
	s_or_b64 exec, exec, s[14:15]
	v_ashrrev_i32_e32 v60, 17, v118
	s_waitcnt vmcnt(3)
	v_mfma_f32_16x16x16_f16 v[52:55], v[72:73], v[44:45], v[56:59]
	v_cmp_ne_u32_e32 vcc, v60, v115
.Lw2t129:
	s_cbranch_execz .Lw2c129
.Lw2b129:
	s_cmp_lg_u64 vcc, 0
	s_cselect_b64 s[14:15], -1, 0
	v_mfma_f32_16x16x16_f16 v[44:47], v[72:73], v[46:47], v[48:51]
	s_and_b64 s[18:19], s[14:15], vcc
	s_and_saveexec_b64 s[14:15], s[18:19]
	s_cbranch_execz .LBB2_80
	v_cmp_gt_i32_e32 vcc, 16, v115
	s_and_saveexec_b64 s[18:19], vcc
	s_cbranch_execz .LBB2_79
	s_nop 1
	v_cvt_pk_f16_f32 v47, v46, v47
	v_cvt_pk_f16_f32 v46, v44, v45

.Lw2b130:
	v_cvt_pk_f16_f32 v45, v54, v55
	v_cvt_pk_f16_f32 v44, v52, v53
	v_mad_u64_u32 v[48:49], s[24:25], v115, s20, v[76:77]
	ds_write_b128 v48, v[44:47]
.LBB2_79:
	s_or_b64 exec, exec, s[18:19]
	s_nop 0
	v_mov_b32_e32 v44, 0
	v_mov_b32_e32 v115, v60
	v_mov_b32_e32 v45, v44
	v_mov_b32_e32 v46, v44
	v_mov_b32_e32 v47, v44
.Lw2t131:
	s_cbranch_execz .Lw2c131
.Lw2b131:
	v_mov_b32_e32 v52, v44
	v_mov_b32_e32 v53, v44
	v_mov_b32_e32 v54, v44
	v_mov_b32_e32 v55, v44
.LBB2_80:
	s_or_b64 exec, exec, s[14:15]
	v_ashrrev_i32_e32 v56, 17, v117
	s_waitcnt vmcnt(2)
	v_mfma_f32_16x16x16_f16 v[48:51], v[72:73], v[40:41], v[52:55]
	v_cmp_ne_u32_e32 vcc, v56, v115
	s_cmp_lg_u64 vcc, 0
	s_cselect_b64 s[14:15], -1, 0
	v_mfma_f32_16x16x16_f16 v[40:43], v[72:73], v[42:43], v[44:47]
	s_and_b64 s[18:19], s[14:15], vcc

.Lw2b132:
	s_and_saveexec_b64 s[14:15], s[18:19]
	s_cbranch_execz .LBB2_84
	v_cmp_gt_i32_e32 vcc, 16, v115
	s_and_saveexec_b64 s[18:19], vcc
	s_cbranch_execz .LBB2_83
	s_nop 1
	v_cvt_pk_f16_f32 v43, v42, v43
	v_cvt_pk_f16_f32 v42, v40, v41
	v_cvt_pk_f16_f32 v41, v50, v51
	v_cvt_pk_f16_f32 v40, v48, v49
	v_mad_u64_u32 v[44:45], s[24:25], v115, s20, v[76:77]

.Lw2b133:
	ds_write_b128 v44, v[40:43]

.LBB2_84:
	s_or_b64 exec, exec, s[14:15]
.Lw2t134:
	s_cbranch_execz .Lw2c134
.Lw2b134:
	v_ashrrev_i32_e32 v52, 17, v116
	s_waitcnt vmcnt(1)
	v_mfma_f32_16x16x16_f16 v[44:47], v[72:73], v[36:37], v[48:51]
	v_cmp_ne_u32_e32 vcc, v52, v115
	s_cmp_lg_u64 vcc, 0
	s_cselect_b64 s[14:15], -1, 0
	v_mfma_f32_16x16x16_f16 v[36:39], v[72:73], v[38:39], v[40:43]
	s_and_b64 s[18:19], s[14:15], vcc
	s_and_saveexec_b64 s[14:15], s[18:19]
	s_cbranch_execz .LBB2_88
	v_cmp_gt_i32_e32 vcc, 16, v115
	s_and_saveexec_b64 s[18:19], vcc
	s_cbranch_execz .LBB2_87

.Lw2b135:
	s_nop 1
	v_cvt_pk_f16_f32 v39, v38, v39
	v_cvt_pk_f16_f32 v38, v36, v37
	v_cvt_pk_f16_f32 v37, v46, v47
	v_cvt_pk_f16_f32 v36, v44, v45
	v_mad_u64_u32 v[40:41], s[24:25], v115, s20, v[76:77]
	ds_write_b128 v40, v[36:39]
.LBB2_87:
	s_or_b64 exec, exec, s[18:19]
	s_nop 0
.Lw2t136:
	s_cbranch_execz .Lw2c136
.Lw2b136:
	v_mov_b32_e32 v36, 0
	v_mov_b32_e32 v115, v52
	v_mov_b32_e32 v37, v36
	v_mov_b32_e32 v38, v36
	v_mov_b32_e32 v39, v36
	v_mov_b32_e32 v44, v36
	v_mov_b32_e32 v45, v36
	v_mov_b32_e32 v46, v36
	v_mov_b32_e32 v47, v36
.LBB2_88:
	s_or_b64 exec, exec, s[14:15]
	s_waitcnt vmcnt(0)
	v_mfma_f32_16x16x16_f16 v[60:63], v[72:73], v[32:33], v[44:47]
	v_add_u32_e32 v32, 16, v113
	v_mfma_f32_16x16x16_f16 v[56:59], v[72:73], v[34:35], v[36:39]
.LBB2_89:
.Lw2t137:
	s_cbranch_execz .Lw2c137
.Lw2b137:
	v_mov_b32_e32 v113, v32
	v_mov_b32_e32 v116, v114
	s_branch .LBB2_20
.LBB2_90:
	v_cmp_gt_i32_e32 vcc, 16, v107
	s_and_saveexec_b64 s[14:15], vcc
	s_cbranch_execz .LBB2_15
	v_cvt_pk_f16_f32 v35, v111, v109
	v_cvt_pk_f16_f32 v34, v112, v110
	v_cvt_pk_f16_f32 v33, v106, v104
	v_cvt_pk_f16_f32 v32, v108, v105

.Lw2b138:
	v_mad_u64_u32 v[36:37], s[16:17], v107, s20, v[76:77]
	ds_write_b128 v36, v[32:35]
	s_branch .LBB2_15

_Z10k_layer_a2ILi1ELi13EEvPKDF16_PKiS3_PK15HIP_vector_typeIjLj4EES7_PKfS9_S9_S9_S9_S9_PDF16_Pf:
	s_load_dwordx4 s[12:15], s[0:1], 0x38

.Lw3b0:
	s_load_dwordx8 s[4:11], s[0:1], 0x18
	v_lshlrev_b32_e32 v2, 4, v0
	v_min_u32_e32 v1, 0x7f, v0
	v_lshlrev_b32_e32 v26, 2, v1
	v_readfirstlane_b32 s3, v0
	v_add_u32_e32 v28, 0x3400, v2
	v_add_u32_e32 v29, 0x6800, v2
	v_add_u32_e32 v30, 0x9c00, v2

.Lw3b1:
	v_add_u32_e32 v31, 0xd00, v0
	v_min_u32_e32 v31, 0xfff, v31
	v_lshlrev_b32_e32 v31, 4, v31
	v_add_u32_e32 v27, 0x680, v0
	v_min_u32_e32 v27, 0x8ff, v27
	v_lshlrev_b32_e32 v27, 4, v27
	s_waitcnt lgkmcnt(0)
	global_load_dwordx4 v[16:19], v2, s[4:5]
	global_load_dwordx4 v[8:11], v28, s[4:5]

.Lw3b2:
	global_load_dwordx4 v[12:15], v29, s[4:5]
	global_load_dwordx4 v[20:23], v30, s[4:5]
	global_load_dwordx4 v[32:35], v31, s[4:5]
	global_load_dwordx4 v[36:39], v2, s[6:7]
	global_load_dwordx4 v[40:43], v28, s[6:7]
	global_load_dwordx4 v[44:47], v27, s[6:7]
	global_load_dword v5, v26, s[8:9]
	global_load_dword v7, v26, s[8:9] offset:512

.Lw3b3:
	global_load_dword v1, v26, s[10:11]
	global_load_dword v4, v26, s[12:13]
	global_load_dword v6, v26, s[14:15]
	s_load_dword s42, s[0:1], 0x0
	s_load_dword s43, s[0:1], 0x40
	v_lshrrev_b32_e32 v48, 6, v0
	s_nop 0
	v_readfirstlane_b32 s41, v48
	s_movk_i32 s40, 0x5aa5
	s_mov_b64 exec, 0
	s_cmpk_lt_u32 s41, 6
	s_cbranch_scc1 .Lw3s0d0_13
	s_cmpk_lt_u32 s41, 9
	s_cbranch_scc1 .Lw3s0d6_13
	s_cmpk_lt_u32 s41, 11
	s_cbranch_scc1 .Lw3s0d9_13
	s_cmpk_lt_u32 s41, 12
	s_cbranch_scc1 .Lw3s0d11_13
	s_branch .Lw3t12

.Lw3e0:
	s_mov_b32 s40, 0
	s_mov_b64 exec, -1
.Lw3t4:
	s_cbranch_execz .Lw3c4
.Lw3b4:
	s_waitcnt vmcnt(12)
	ds_write_b128 v2, v[16:19]
	s_waitcnt vmcnt(11)
	ds_write_b128 v2, v[8:11] offset:13312
	s_waitcnt vmcnt(10)

.Lw3b5:
	ds_write_b128 v2, v[12:15] offset:26624
	s_waitcnt vmcnt(9)
	ds_write_b128 v2, v[20:23] offset:39936
	s_movk_i32 s4, 0x300
	v_cmp_gt_u32_e32 vcc, s4, v0
	s_waitcnt vmcnt(8)
	s_and_saveexec_b64 s[4:5], vcc
	ds_write_b128 v2, v[32:35] offset:53248
	s_or_b64 exec, exec, s[4:5]
	v_mov_b32_e32 v3, 0x1dd00
	v_lshl_add_u32 v3, v0, 4, v3

.Lw3b6:
	s_waitcnt vmcnt(7)
	ds_write_b128 v3, v[36:39]
	s_waitcnt vmcnt(6)
	ds_write_b128 v3, v[40:43] offset:13312
	s_movk_i32 s4, 0x280
	v_cmp_gt_u32_e32 vcc, s4, v0
	s_waitcnt vmcnt(5)
	s_and_saveexec_b64 s[4:5], vcc
	ds_write_b128 v3, v[44:47] offset:26624
	s_or_b64 exec, exec, s[4:5]
	s_waitcnt vmcnt(0)

.Lw3b7:
	s_movk_i32 s4, 0x80
	v_cmp_gt_u32_e32 vcc, s4, v0
	s_and_saveexec_b64 s[4:5], vcc
	s_cbranch_execz .LBB3_6
	v_mov_b32_e32 v3, 0x26d00
	v_add_f32_e32 v2, v5, v7
	v_lshl_add_u32 v3, v0, 2, v3
	ds_write2st64_b32 v3, v2, v1 offset1:2
	ds_write2st64_b32 v3, v4, v6 offset0:4 offset1:6
.LBB3_6:
	s_or_b64 exec, exec, s[4:5]
	s_load_dwordx2 s[6:7], s[0:1], 0x60
.Lw3t8:
	s_cbranch_execz .Lw3c8
.Lw3b8:
	s_load_dwordx2 s[16:17], s[0:1], 0x50
	s_load_dwordx4 s[8:11], s[0:1], 0x0
	s_load_dwordx2 s[18:19], s[0:1], 0x10
	s_mov_b32 s13, 0
	v_cmp_eq_u32_e32 vcc, 0, v0
	s_and_saveexec_b64 s[4:5], vcc
	v_mov_b32_e32 v1, 0
	v_mov_b32_e32 v2, 0x27900
	ds_write_b32 v2, v1

.Lw3b9:
	s_or_b64 exec, exec, s[4:5]
	v_bfe_u32 v1, v0, 4, 2
	v_bfe_u32 v2, v0, 2, 2
	v_cmp_eq_u32_e32 vcc, v1, v2
	v_and_b32_e32 v2, 3, v0
	v_cmp_eq_u32_e64 s[4:5], 0, v2
	v_mov_b32_e32 v3, 0x3c00
	s_and_b64 s[4:5], vcc, s[4:5]
	v_cndmask_b32_e64 v4, 0, v3, s[4:5]
	v_cmp_eq_u32_e64 s[4:5], 1, v2

.Lw3b10:
	s_and_b64 s[4:5], vcc, s[4:5]
	s_lshr_b32 s12, s3, 6
	v_cndmask_b32_e64 v5, 0, v3, s[4:5]
	v_cmp_eq_u32_e64 s[4:5], 2, v2
	s_and_b64 s[4:5], vcc, s[4:5]
	v_and_b32_e32 v77, 63, v0
	v_cndmask_b32_e64 v6, 0, v3, s[4:5]
	v_cmp_eq_u32_e64 s[4:5], 3, v2
	s_and_b64 vcc, vcc, s[4:5]
	v_cndmask_b32_e32 v2, 0, v3, vcc

.Lw3b11:
	v_pack_b32_f16 v73, v6, v2
	v_lshlrev_b32_e32 v2, 2, v0
	v_and_b32_e32 v82, 0xc0, v2
	v_and_b32_e32 v2, 48, v0
	v_mov_b32_e32 v3, 0
	s_waitcnt lgkmcnt(0)
	s_barrier
	v_and_b32_e32 v80, 15, v0
	s_load_dword s3, s[0:1], 0x68
	s_mul_i32 s0, s12, 0x1100
	v_lshl_add_u64 v[74:75], s[10:11], 0, v[2:3]

.Lw3b12:
	v_bfe_u32 v3, v0, 2, 4
	v_lshlrev_b32_e32 v0, 6, v0
	s_add_i32 s4, s0, 0x10000
	v_mul_u32_u24_e32 v3, 0x110, v3
	v_and_b32_e32 v0, 0xc0, v0
	s_movk_i32 s26, 0x110
	v_add3_u32 v83, s4, v3, v0
	v_mov_b32_e32 v0, s4
	v_mad_u32_u24 v0, v80, s26, v0

.Lw3b13:
	v_pack_b32_f16 v72, v4, v5
	v_lshlrev_b32_e32 v81, 4, v80
	v_lshlrev_b32_e32 v4, 7, v1
	v_add_u32_e32 v97, v0, v2
	v_mbcnt_lo_u32_b32 v0, -1, 0
	v_cmp_eq_u32_e64 s[0:1], 0, v77
	v_or_b32_e32 v76, s4, v81
	v_lshlrev_b32_e32 v84, 5, v1
	v_cmp_gt_u32_e64 s[4:5], 16, v77
	v_or_b32_e32 v85, 24, v82

.Lw3b14:
	v_or_b32_e32 v86, 28, v82
	v_or_b32_e32 v87, 32, v82
	v_or_b32_e32 v88, 36, v82
	v_or_b32_e32 v89, 40, v82
	v_or_b32_e32 v90, 44, v82
	v_or_b32_e32 v91, 48, v82
	v_or_b32_e32 v92, 52, v82
	v_or_b32_e32 v93, 56, v82
	v_or_b32_e32 v94, 60, v82
	v_mov_b32_e32 v95, 0x27900
	v_add_u32_e32 v96, 0x26d00, v4
	s_mov_b32 s27, 0x1ffff00

.Lw3b15:
	v_mov_b32_e32 v98, 0x3727c5ac
	s_mov_b32 s28, 0x800000
	v_mov_b32_e32 v99, 0xc0135761
	v_mbcnt_hi_u32_b32 v100, -1, v0
	v_mov_b32_e32 v101, 0x26d00
	v_mov_b32_e32 v102, 0x1dd00
	s_branch .LBB3_11
.LBB3_9:
	s_or_b64 exec, exec, s[14:15]
	s_mov_b64 s[10:11], 0
.LBB3_10:
.Lw3t16:
	s_cbranch_execz .Lw3c16
.Lw3b16:
	s_and_b64 vcc, exec, s[10:11]
	s_cbranch_vccnz .LBB3_96
.LBB3_11:
	s_nop 0
	v_mov_b32_e32 v0, 0
	s_and_saveexec_b64 s[10:11], s[0:1]
	s_cbranch_execz .LBB3_15
	s_mov_b64 s[20:21], exec
	v_mbcnt_lo_u32_b32 v0, s20, 0
	v_mbcnt_hi_u32_b32 v0, s21, v0
	v_cmp_eq_u32_e32 vcc, 0, v0
	s_and_saveexec_b64 s[14:15], vcc
	s_bcnt1_i32_b64 s12, s[20:21]
	v_mov_b32_e32 v1, s12
.Lw3t17:
	s_cbranch_execz .Lw3c17
.Lw3b17:
	ds_add_rtn_u32 v1, v95, v1
	s_or_b64 exec, exec, s[14:15]
	s_waitcnt lgkmcnt(0)
	v_readfirstlane_b32 s12, v1
	s_nop 1
	v_add_u32_e32 v0, s12, v0
.LBB3_15:
	s_or_b64 exec, exec, s[10:11]
	v_readfirstlane_b32 s10, v0
	s_waitcnt lgkmcnt(0)
	s_mul_i32 s12, s10, s3
	s_add_i32 s12, s12, s2
	s_cmpk_gt_i32 s12, 0x1869
	s_mov_b64 s[10:11], -1
	s_cbranch_scc1 .LBB3_10
.Lw3t18:
	s_cbranch_execz .Lw3c18
.Lw3b18:
	ds_read_b128 v[28:31], v96
	ds_read_b128 v[24:27], v96 offset:16
	ds_read_b128 v[20:23], v96 offset:32
	ds_read_b128 v[16:19], v96 offset:48
	ds_read_b128 v[12:15], v96 offset:64
	ds_read_b128 v[8:11], v96 offset:80
	ds_read_b128 v[4:7], v96 offset:96
	ds_read_b128 v[0:3], v96 offset:112

.Lw3b19:
	s_lshl_b32 s10, s12, 4
	s_ashr_i32 s11, s10, 31
	v_lshl_add_u64 v[78:79], s[10:11], 2, v[74:75]
	s_mov_b32 s11, 0
	s_mov_b64 s[22:23], -1
	s_branch .LBB3_18
.LBB3_17:
	s_or_b64 exec, exec, s[20:21]
	v_mov_b32_e32 v48, v77
	ds_read_b128 v[32:35], v97
	ds_read_b128 v[36:39], v97 offset:64
	ds_read_b128 v[40:43], v97 offset:128
.Lw3t20:
	s_cbranch_execz .Lw3c20
.Lw3b20:
	ds_read_b128 v[44:47], v97 offset:192
	s_nop 0
	v_lshlrev_b32_e32 v48, 4, v48
	v_lshl_add_u32 v103, s11, 15, v48
	ds_read_b128 v[48:51], v103
	ds_read_b128 v[52:55], v103 offset:1024
	ds_read_b128 v[56:59], v103 offset:2048
	ds_read_b128 v[60:63], v103 offset:3072

.Lw3b31:
	v_mfma_f32_16x16x32_f16 v[0:3], v[64:67], v[44:47], v[0:3]
	s_mov_b32 s11, 1
	s_mov_b64 s[22:23], 0
	s_and_b64 vcc, exec, s[14:15]
	s_cbranch_vccnz .LBB3_94
.LBB3_18:
	s_mul_i32 s12, s11, 0x186a1
	v_lshl_add_u64 v[32:33], s[12:13], 2, v[78:79]
	global_load_dword v113, v[32:33], off
	global_load_dword v103, v[32:33], off offset:16
	s_mov_b32 s14, s13
.Lw3t32:
	s_cbranch_execz .Lw3c32
.Lw3b32:
	s_mov_b32 s15, s13
	s_mul_i32 s12, s11, 0xc3500
	s_lshl_b64 s[20:21], s[12:13], 2
	s_mov_b32 s12, s13
	v_mov_b64_e32 v[34:35], s[14:15]
	v_mov_b64_e32 v[32:33], s[12:13]
	s_add_u32 s20, s18, s20
	ds_write_b128 v83, v[32:35]
	ds_write_b128 v83, v[32:35] offset:16
	ds_write_b128 v83, v[32:35] offset:32
	ds_write_b128 v83, v[32:35] offset:48
	s_addc_u32 s21, s19, s21

.Lw3b33:
	v_mov_b32_e32 v116, 0x3f86a0
	s_waitcnt vmcnt(1)
	v_add_u32_e32 v32, v113, v80
	s_waitcnt vmcnt(0)
	v_cmp_lt_i32_e32 vcc, v32, v103
	s_and_saveexec_b64 s[14:15], vcc
	s_cbranch_execz .LBB3_20
	v_ashrrev_i32_e32 v33, 31, v32
	v_lshl_add_u64 v[32:33], v[32:33], 2, s[20:21]
	global_load_dword v116, v[32:33], off
.LBB3_20:
.Lw3t34:
	s_cbranch_execz .Lw3c34

.LBB3_21:
	s_waitcnt vmcnt(0)
	v_mov_b32_e32 v116, v114
	s_cbranch_execnz .LBB3_92
.LBB3_22:
.Lw3t35:
	s_cbranch_execz .Lw3c35
.Lw3b35:
	s_nop 2
	v_mov_b32_e32 v104, v63
	v_mov_b32_e32 v106, v62
	v_mov_b32_e32 v105, v61
	v_mov_b32_e32 v108, v60
	v_mov_b32_e32 v109, v59
	v_mov_b32_e32 v111, v58
	v_mov_b32_e32 v110, v57
	v_mov_b32_e32 v112, v56
	v_mov_b32_e32 v107, v115
	v_cmp_lt_i32_e32 vcc, v113, v103
	s_cbranch_vccz .LBB3_21
	v_or_b32_e32 v32, 4, v82
	s_waitcnt vmcnt(0)
	ds_bpermute_b32 v66, v82, v116

.Lw3b36:
	ds_bpermute_b32 v123, v32, v116
	v_or_b32_e32 v32, 8, v82
	v_or_b32_e32 v34, 12, v82
	ds_bpermute_b32 v122, v32, v116
	ds_bpermute_b32 v121, v34, v116
	v_or_b32_e32 v34, 16, v82
	ds_bpermute_b32 v120, v34, v116
	v_or_b32_e32 v34, 20, v82
	ds_bpermute_b32 v119, v34, v116

.Lw3b37:
	s_waitcnt lgkmcnt(5)
	v_lshlrev_b32_e32 v32, 8, v66
	s_waitcnt lgkmcnt(4)
	v_lshlrev_b32_e32 v33, 8, v123
	v_and_or_b32 v32, v32, s27, v81
	v_and_or_b32 v33, v33, s27, v81
	ds_bpermute_b32 v118, v85, v116
	ds_bpermute_b32 v117, v86, v116
	global_load_dwordx4 v[60:63], v32, s[8:9]
	global_load_dwordx4 v[56:59], v33, s[8:9]

.Lw3b38:
	s_waitcnt lgkmcnt(5)
	v_lshlrev_b32_e32 v32, 8, v122
	s_waitcnt lgkmcnt(4)
	v_lshlrev_b32_e32 v33, 8, v121
	v_and_or_b32 v32, v32, s27, v81
	v_and_or_b32 v33, v33, s27, v81
	global_load_dwordx4 v[52:55], v32, s[8:9]
	global_load_dwordx4 v[48:51], v33, s[8:9]
	s_waitcnt lgkmcnt(3)
	v_lshlrev_b32_e32 v32, 8, v120

.Lw3b39:
	s_waitcnt lgkmcnt(2)
	v_lshlrev_b32_e32 v33, 8, v119
	v_and_or_b32 v32, v32, s27, v81
	v_and_or_b32 v33, v33, s27, v81
	global_load_dwordx4 v[44:47], v32, s[8:9]
	global_load_dwordx4 v[40:43], v33, s[8:9]
	s_waitcnt lgkmcnt(1)
	v_lshlrev_b32_e32 v32, 8, v118
	s_waitcnt lgkmcnt(0)
	v_lshlrev_b32_e32 v33, 8, v117
	v_and_or_b32 v32, v32, s27, v81

.Lw3b40:
	v_and_or_b32 v33, v33, s27, v81
	global_load_dwordx4 v[36:39], v32, s[8:9]
	s_nop 0
	global_load_dwordx4 v[32:35], v33, s[8:9]
	v_or_b32_e32 v64, 16, v80
	v_add_u32_e32 v64, v64, v113
	v_cmp_lt_i32_e32 vcc, v64, v103
	v_mov_b32_e32 v114, 0x3f86a0
	s_and_saveexec_b64 s[22:23], vcc
	s_cbranch_execz .LBB3_25

.Lw3b41:
	v_ashrrev_i32_e32 v65, 31, v64
	v_lshl_add_u64 v[64:65], v[64:65], 2, s[20:21]
	global_load_dword v114, v[64:65], off
.LBB3_25:
	s_or_b64 exec, exec, s[22:23]
	v_ashrrev_i32_e32 v124, 17, v66
	v_cmp_ne_u32_e32 vcc, v124, v107
	s_cmp_lg_u64 vcc, 0
	s_cselect_b64 s[22:23], -1, 0
	s_and_b64 s[24:25], s[22:23], vcc
	v_mov_b32_e32 v115, v107
	v_mov_b32_e32 v68, v112
	v_mov_b32_e32 v69, v110
	v_mov_b32_e32 v70, v111
.Lw3t42:
	s_cbranch_execz .Lw3c42
.Lw3b42:
	v_mov_b32_e32 v71, v109
	v_mov_b32_e32 v64, v108
	v_mov_b32_e32 v65, v105
	v_mov_b32_e32 v66, v106
	v_mov_b32_e32 v67, v104
	s_and_saveexec_b64 s[22:23], s[24:25]
	s_cbranch_execz .LBB3_29
	v_cmp_gt_i32_e32 vcc, 16, v107
	s_and_saveexec_b64 s[24:25], vcc
	s_cbranch_execz .LBB3_28
	v_cvt_pk_f16_f32 v67, v111, v109
	v_cvt_pk_f16_f32 v66, v112, v110
	v_cvt_pk_f16_f32 v65, v106, v104

.Lw3b43:
	v_cvt_pk_f16_f32 v64, v108, v105
	v_mad_u64_u32 v[68:69], s[30:31], v107, s26, v[76:77]
	ds_write_b128 v68, v[64:67]
.LBB3_28:
	s_or_b64 exec, exec, s[24:25]
	v_mov_b32_e32 v68, 0
	v_mov_b32_e32 v115, v124
	v_mov_b32_e32 v69, v68
	v_mov_b32_e32 v70, v68
	v_mov_b32_e32 v71, v68
	v_mov_b32_e32 v64, v68
	v_mov_b32_e32 v65, v68
.Lw3t44:
	s_cbranch_execz .Lw3c44
.Lw3b44:
	v_mov_b32_e32 v66, v68
	v_mov_b32_e32 v67, v68
.LBB3_29:
	s_or_b64 exec, exec, s[22:23]
	v_ashrrev_i32_e32 v123, 17, v123
	s_waitcnt vmcnt(7)
	v_mfma_f32_16x16x16_f16 v[64:67], v[72:73], v[60:61], v[64:67]
	v_cmp_ne_u32_e32 vcc, v123, v115
	s_cmp_lg_u64 vcc, 0
	s_cselect_b64 s[22:23], -1, 0
	v_mfma_f32_16x16x16_f16 v[60:63], v[72:73], v[62:63], v[68:71]
	s_and_b64 s[24:25], s[22:23], vcc
	s_and_saveexec_b64 s[22:23], s[24:25]
	s_cbranch_execz .LBB3_33
.Lw3t45:
	s_cbranch_execz .Lw3c45
.Lw3b45:
	v_cmp_gt_i32_e32 vcc, 16, v115
	s_and_saveexec_b64 s[24:25], vcc
	s_cbranch_execz .LBB3_32
	s_nop 1
	v_cvt_pk_f16_f32 v63, v62, v63
	v_cvt_pk_f16_f32 v62, v60, v61
	v_cvt_pk_f16_f32 v61, v66, v67
	v_cvt_pk_f16_f32 v60, v64, v65
	v_mad_u64_u32 v[64:65], s[30:31], v115, s26, v[76:77]
	ds_write_b128 v64, v[60:63]

.LBB3_33:
	s_or_b64 exec, exec, s[22:23]
	v_ashrrev_i32_e32 v68, 17, v122
	s_waitcnt vmcnt(6)
.Lw3t47:
	s_cbranch_execz .Lw3c47
.Lw3b47:
	v_mfma_f32_16x16x16_f16 v[64:67], v[72:73], v[56:57], v[64:67]
	v_cmp_ne_u32_e32 vcc, v68, v115
	s_cmp_lg_u64 vcc, 0
	s_cselect_b64 s[22:23], -1, 0
	v_mfma_f32_16x16x16_f16 v[56:59], v[72:73], v[58:59], v[60:63]
	s_and_b64 s[24:25], s[22:23], vcc
	s_and_saveexec_b64 s[22:23], s[24:25]
	s_cbranch_execz .LBB3_37
	v_cmp_gt_i32_e32 vcc, 16, v115
	s_and_saveexec_b64 s[24:25], vcc
	s_cbranch_execz .LBB3_36
	s_nop 1
	v_cvt_pk_f16_f32 v59, v58, v59

.Lw3b48:
	v_cvt_pk_f16_f32 v58, v56, v57
	v_cvt_pk_f16_f32 v57, v66, v67
	v_cvt_pk_f16_f32 v56, v64, v65
	v_mad_u64_u32 v[60:61], s[30:31], v115, s26, v[76:77]
	ds_write_b128 v60, v[56:59]
.LBB3_36:
	s_or_b64 exec, exec, s[24:25]
	s_nop 0
	v_mov_b32_e32 v56, 0
	v_mov_b32_e32 v115, v68
.Lw3t49:
	s_cbranch_execz .Lw3c49
.Lw3b49:
	v_mov_b32_e32 v57, v56
	v_mov_b32_e32 v58, v56
	v_mov_b32_e32 v59, v56
	v_mov_b32_e32 v64, v56
	v_mov_b32_e32 v65, v56
	v_mov_b32_e32 v66, v56
	v_mov_b32_e32 v67, v56
.LBB3_37:
	s_or_b64 exec, exec, s[22:23]
	v_ashrrev_i32_e32 v68, 17, v121
	s_waitcnt vmcnt(5)
	v_mfma_f32_16x16x16_f16 v[60:63], v[72:73], v[52:53], v[64:67]
	v_cmp_ne_u32_e32 vcc, v68, v115
	s_cmp_lg_u64 vcc, 0
	s_cselect_b64 s[22:23], -1, 0
.Lw3t50:
	s_cbranch_execz .Lw3c50
.Lw3b50:
	v_mfma_f32_16x16x16_f16 v[52:55], v[72:73], v[54:55], v[56:59]
	s_and_b64 s[24:25], s[22:23], vcc
	s_and_saveexec_b64 s[22:23], s[24:25]
	s_cbranch_execz .LBB3_41
	v_cmp_gt_i32_e32 vcc, 16, v115
	s_and_saveexec_b64 s[24:25], vcc
	s_cbranch_execz .LBB3_40
	s_nop 1
	v_cvt_pk_f16_f32 v55, v54, v55
	v_cvt_pk_f16_f32 v54, v52, v53
	v_cvt_pk_f16_f32 v53, v62, v63

.Lw3b51:
	v_cvt_pk_f16_f32 v52, v60, v61
	v_mad_u64_u32 v[56:57], s[30:31], v115, s26, v[76:77]
	ds_write_b128 v56, v[52:55]
.LBB3_40:
	s_or_b64 exec, exec, s[24:25]
	s_nop 0
	v_mov_b32_e32 v52, 0
	v_mov_b32_e32 v115, v68
	v_mov_b32_e32 v53, v52
	v_mov_b32_e32 v54, v52
	v_mov_b32_e32 v55, v52
	v_mov_b32_e32 v60, v52
	v_mov_b32_e32 v61, v52
.Lw3t52:
	s_cbranch_execz .Lw3c52
.Lw3b52:
	v_mov_b32_e32 v62, v52
	v_mov_b32_e32 v63, v52
.LBB3_41:
	s_or_b64 exec, exec, s[22:23]
	v_ashrrev_i32_e32 v64, 17, v120
	s_waitcnt vmcnt(4)
	v_mfma_f32_16x16x16_f16 v[56:59], v[72:73], v[48:49], v[60:63]
	v_cmp_ne_u32_e32 vcc, v64, v115
	s_cmp_lg_u64 vcc, 0
	s_cselect_b64 s[22:23], -1, 0
	v_mfma_f32_16x16x16_f16 v[48:51], v[72:73], v[50:51], v[52:55]
	s_and_b64 s[24:25], s[22:23], vcc
	s_and_saveexec_b64 s[22:23], s[24:25]
	s_cbranch_execz .LBB3_45
.Lw3t53:
	s_cbranch_execz .Lw3c53
.Lw3b53:
	v_cmp_gt_i32_e32 vcc, 16, v115
	s_and_saveexec_b64 s[24:25], vcc
	s_cbranch_execz .LBB3_44
	s_nop 1
	v_cvt_pk_f16_f32 v51, v50, v51
	v_cvt_pk_f16_f32 v50, v48, v49
	v_cvt_pk_f16_f32 v49, v58, v59
	v_cvt_pk_f16_f32 v48, v56, v57
	v_mad_u64_u32 v[52:53], s[30:31], v115, s26, v[76:77]
	ds_write_b128 v52, v[48:51]

.LBB3_45:
	s_or_b64 exec, exec, s[22:23]
	v_ashrrev_i32_e32 v60, 17, v119
	s_waitcnt vmcnt(3)
.Lw3t55:
	s_cbranch_execz .Lw3c55
.Lw3b55:
	v_mfma_f32_16x16x16_f16 v[52:55], v[72:73], v[44:45], v[56:59]
	v_cmp_ne_u32_e32 vcc, v60, v115
	s_cmp_lg_u64 vcc, 0
	s_cselect_b64 s[22:23], -1, 0
	v_mfma_f32_16x16x16_f16 v[44:47], v[72:73], v[46:47], v[48:51]
	s_and_b64 s[24:25], s[22:23], vcc
	s_and_saveexec_b64 s[22:23], s[24:25]
	s_cbranch_execz .LBB3_49
	v_cmp_gt_i32_e32 vcc, 16, v115
	s_and_saveexec_b64 s[24:25], vcc
	s_cbranch_execz .LBB3_48
	s_nop 1
	v_cvt_pk_f16_f32 v47, v46, v47

.Lw3b56:
	v_cvt_pk_f16_f32 v46, v44, v45
	v_cvt_pk_f16_f32 v45, v54, v55
	v_cvt_pk_f16_f32 v44, v52, v53
	v_mad_u64_u32 v[48:49], s[30:31], v115, s26, v[76:77]
	ds_write_b128 v48, v[44:47]
.LBB3_48:
	s_or_b64 exec, exec, s[24:25]
	s_nop 0
	v_mov_b32_e32 v44, 0
	v_mov_b32_e32 v115, v60
.Lw3t57:
	s_cbranch_execz .Lw3c57
.Lw3b57:
	v_mov_b32_e32 v45, v44
	v_mov_b32_e32 v46, v44
	v_mov_b32_e32 v47, v44
	v_mov_b32_e32 v52, v44
	v_mov_b32_e32 v53, v44
	v_mov_b32_e32 v54, v44
	v_mov_b32_e32 v55, v44
.LBB3_49:
	s_or_b64 exec, exec, s[22:23]
	v_ashrrev_i32_e32 v56, 17, v118
	s_waitcnt vmcnt(2)
	v_mfma_f32_16x16x16_f16 v[48:51], v[72:73], v[40:41], v[52:55]
	v_cmp_ne_u32_e32 vcc, v56, v115
	s_cmp_lg_u64 vcc, 0
	s_cselect_b64 s[22:23], -1, 0
.Lw3t58:
	s_cbranch_execz .Lw3c58
.Lw3b58:
	v_mfma_f32_16x16x16_f16 v[40:43], v[72:73], v[42:43], v[44:47]
	s_and_b64 s[24:25], s[22:23], vcc
	s_and_saveexec_b64 s[22:23], s[24:25]
	s_cbranch_execz .LBB3_53
	v_cmp_gt_i32_e32 vcc, 16, v115
	s_and_saveexec_b64 s[24:25], vcc
	s_cbranch_execz .LBB3_52
	s_nop 1
	v_cvt_pk_f16_f32 v43, v42, v43
	v_cvt_pk_f16_f32 v42, v40, v41
	v_cvt_pk_f16_f32 v41, v50, v51

.Lw3b59:
	v_cvt_pk_f16_f32 v40, v48, v49
	v_mad_u64_u32 v[44:45], s[30:31], v115, s26, v[76:77]
	ds_write_b128 v44, v[40:43]
.LBB3_52:
	s_or_b64 exec, exec, s[24:25]
	s_nop 0
	v_mov_b32_e32 v40, 0
	v_mov_b32_e32 v115, v56
	v_mov_b32_e32 v41, v40
	v_mov_b32_e32 v42, v40
	v_mov_b32_e32 v43, v40
	v_mov_b32_e32 v48, v40
	v_mov_b32_e32 v49, v40
.Lw3t60:
	s_cbranch_execz .Lw3c60
.Lw3b60:
	v_mov_b32_e32 v50, v40
	v_mov_b32_e32 v51, v40
.LBB3_53:
	s_or_b64 exec, exec, s[22:23]
	v_ashrrev_i32_e32 v52, 17, v117
	s_waitcnt vmcnt(1)
	v_mfma_f32_16x16x16_f16 v[44:47], v[72:73], v[36:37], v[48:51]
	v_cmp_ne_u32_e32 vcc, v52, v115
	s_cmp_lg_u64 vcc, 0
	s_cselect_b64 s[22:23], -1, 0
	v_mfma_f32_16x16x16_f16 v[36:39], v[72:73], v[38:39], v[40:43]
	s_and_b64 s[24:25], s[22:23], vcc
	s_and_saveexec_b64 s[22:23], s[24:25]
	s_cbranch_execz .LBB3_57
.Lw3t61:
	s_cbranch_execz .Lw3c61
.Lw3b61:
	v_cmp_gt_i32_e32 vcc, 16, v115
	s_and_saveexec_b64 s[24:25], vcc
	s_cbranch_execz .LBB3_56
	s_nop 1
	v_cvt_pk_f16_f32 v39, v38, v39
	v_cvt_pk_f16_f32 v38, v36, v37
	v_cvt_pk_f16_f32 v37, v46, v47
	v_cvt_pk_f16_f32 v36, v44, v45
	v_mad_u64_u32 v[40:41], s[30:31], v115, s26, v[76:77]
	ds_write_b128 v40, v[36:39]

.LBB3_57:
	s_or_b64 exec, exec, s[22:23]
	s_waitcnt vmcnt(0)
	v_mfma_f32_16x16x16_f16 v[60:63], v[72:73], v[32:33], v[44:47]
.Lw3t63:
	s_cbranch_execz .Lw3c63
.Lw3b63:
	v_add_u32_e32 v32, 8, v113
	v_cmp_lt_i32_e32 vcc, v32, v103
	v_mfma_f32_16x16x16_f16 v[56:59], v[72:73], v[34:35], v[36:39]
	s_cbranch_vccz .LBB3_91
	ds_bpermute_b32 v123, v87, v116
	ds_bpermute_b32 v122, v88, v116
	ds_bpermute_b32 v121, v89, v116
	ds_bpermute_b32 v120, v90, v116
	ds_bpermute_b32 v119, v91, v116

.Lw3b64:
	ds_bpermute_b32 v118, v92, v116
	s_waitcnt lgkmcnt(5)
	v_lshlrev_b32_e32 v32, 8, v123
	s_waitcnt lgkmcnt(4)
	v_lshlrev_b32_e32 v33, 8, v122
	v_and_or_b32 v32, v32, s27, v81
	v_and_or_b32 v33, v33, s27, v81
	ds_bpermute_b32 v117, v93, v116
	ds_bpermute_b32 v116, v94, v116

.Lw3b65:
	global_load_dwordx4 v[68:71], v32, s[8:9]
	global_load_dwordx4 v[64:67], v33, s[8:9]
	s_waitcnt lgkmcnt(5)
	v_lshlrev_b32_e32 v32, 8, v121
	s_waitcnt lgkmcnt(4)
	v_lshlrev_b32_e32 v33, 8, v120
	v_and_or_b32 v32, v32, s27, v81
	v_and_or_b32 v33, v33, s27, v81
	global_load_dwordx4 v[52:55], v32, s[8:9]
	global_load_dwordx4 v[48:51], v33, s[8:9]

.Lw3b66:
	s_waitcnt lgkmcnt(3)
	v_lshlrev_b32_e32 v32, 8, v119
	s_waitcnt lgkmcnt(2)
	v_lshlrev_b32_e32 v33, 8, v118
	v_and_or_b32 v32, v32, s27, v81
	v_and_or_b32 v33, v33, s27, v81
	global_load_dwordx4 v[44:47], v32, s[8:9]
	global_load_dwordx4 v[40:43], v33, s[8:9]
	s_waitcnt lgkmcnt(1)
	v_lshlrev_b32_e32 v32, 8, v117

.Lw3b67:
	s_waitcnt lgkmcnt(0)
	v_lshlrev_b32_e32 v33, 8, v116
	v_and_or_b32 v32, v32, s27, v81
	v_and_or_b32 v33, v33, s27, v81
	global_load_dwordx4 v[36:39], v32, s[8:9]
	s_nop 0
	global_load_dwordx4 v[32:35], v33, s[8:9]
	v_ashrrev_i32_e32 v123, 17, v123
	v_cmp_ne_u32_e32 vcc, v123, v115
	s_cmp_lg_u64 vcc, 0
	s_cselect_b64 s[22:23], -1, 0

.Lw3b68:
	s_and_b64 s[24:25], s[22:23], vcc
	s_and_saveexec_b64 s[22:23], s[24:25]
	s_cbranch_execz .LBB3_62
	v_cmp_gt_i32_e32 vcc, 16, v115
	s_and_saveexec_b64 s[24:25], vcc
	s_cbranch_execz .LBB3_61
	v_cvt_pk_f16_f32 v59, v58, v59
	v_cvt_pk_f16_f32 v58, v56, v57
	v_cvt_pk_f16_f32 v57, v62, v63
	v_cvt_pk_f16_f32 v56, v60, v61
	v_mad_u64_u32 v[60:61], s[30:31], v115, s26, v[76:77]

.LBB3_62:
	s_or_b64 exec, exec, s[22:23]
	v_ashrrev_i32_e32 v122, 17, v122
.Lw3t70:
	s_cbranch_execz .Lw3c70
.Lw3b70:
	s_waitcnt vmcnt(7)
	v_mfma_f32_16x16x16_f16 v[60:63], v[72:73], v[68:69], v[60:63]
	v_cmp_ne_u32_e32 vcc, v122, v115
	s_cmp_lg_u64 vcc, 0
	s_cselect_b64 s[22:23], -1, 0
	v_mfma_f32_16x16x16_f16 v[56:59], v[72:73], v[70:71], v[56:59]
	s_and_b64 s[24:25], s[22:23], vcc
	s_and_saveexec_b64 s[22:23], s[24:25]
	s_cbranch_execz .LBB3_66
	v_cmp_gt_i32_e32 vcc, 16, v115
	s_and_saveexec_b64 s[24:25], vcc
	s_cbranch_execz .LBB3_65
	s_nop 1

.Lw3b71:
	v_cvt_pk_f16_f32 v59, v58, v59
	v_cvt_pk_f16_f32 v58, v56, v57
	v_cvt_pk_f16_f32 v57, v62, v63
	v_cvt_pk_f16_f32 v56, v60, v61
	v_mad_u64_u32 v[60:61], s[30:31], v115, s26, v[76:77]
	ds_write_b128 v60, v[56:59]
.LBB3_65:
	s_or_b64 exec, exec, s[24:25]
	s_nop 0
	v_mov_b32_e32 v56, 0
.Lw3t72:
	s_cbranch_execz .Lw3c72
.Lw3b72:
	v_mov_b32_e32 v115, v122
	v_mov_b32_e32 v57, v56
	v_mov_b32_e32 v58, v56
	v_mov_b32_e32 v59, v56
	v_mov_b32_e32 v60, v56
	v_mov_b32_e32 v61, v56
	v_mov_b32_e32 v62, v56
	v_mov_b32_e32 v63, v56
.LBB3_66:
	s_or_b64 exec, exec, s[22:23]
	v_ashrrev_i32_e32 v68, 17, v121
	s_waitcnt vmcnt(6)
	v_mfma_f32_16x16x16_f16 v[60:63], v[72:73], v[64:65], v[60:63]
	v_cmp_ne_u32_e32 vcc, v68, v115
	s_cmp_lg_u64 vcc, 0
	s_cselect_b64 s[22:23], -1, 0
.Lw3t73:
	s_cbranch_execz .Lw3c73
.Lw3b73:
	v_mfma_f32_16x16x16_f16 v[56:59], v[72:73], v[66:67], v[56:59]
	s_and_b64 s[24:25], s[22:23], vcc
	s_and_saveexec_b64 s[22:23], s[24:25]
	s_cbranch_execz .LBB3_70
	v_cmp_gt_i32_e32 vcc, 16, v115
	s_and_saveexec_b64 s[24:25], vcc
	s_cbranch_execz .LBB3_69
	s_nop 1
	v_cvt_pk_f16_f32 v59, v58, v59
	v_cvt_pk_f16_f32 v58, v56, v57
	v_cvt_pk_f16_f32 v57, v62, v63

.LBB3_69:
	s_or_b64 exec, exec, s[24:25]
	s_nop 0
	v_mov_b32_e32 v56, 0
	v_mov_b32_e32 v115, v68
	v_mov_b32_e32 v57, v56
	v_mov_b32_e32 v58, v56
	v_mov_b32_e32 v59, v56
	v_mov_b32_e32 v60, v56
.Lw3t75:
	s_cbranch_execz .Lw3c75
.Lw3b75:
	v_mov_b32_e32 v61, v56
	v_mov_b32_e32 v62, v56
	v_mov_b32_e32 v63, v56
.LBB3_70:
	s_or_b64 exec, exec, s[22:23]
	v_ashrrev_i32_e32 v64, 17, v120
	s_waitcnt vmcnt(5)
	v_mfma_f32_16x16x16_f16 v[60:63], v[72:73], v[52:53], v[60:63]
	v_cmp_ne_u32_e32 vcc, v64, v115
	s_cmp_lg_u64 vcc, 0
	s_cselect_b64 s[22:23], -1, 0
	v_mfma_f32_16x16x16_f16 v[52:55], v[72:73], v[54:55], v[56:59]
	s_and_b64 s[24:25], s[22:23], vcc
	s_and_saveexec_b64 s[22:23], s[24:25]
.Lw3t76:
	s_cbranch_execz .Lw3c76
.Lw3b76:
	s_cbranch_execz .LBB3_74
	v_cmp_gt_i32_e32 vcc, 16, v115
	s_and_saveexec_b64 s[24:25], vcc
	s_cbranch_execz .LBB3_73
	s_nop 1
	v_cvt_pk_f16_f32 v55, v54, v55
	v_cvt_pk_f16_f32 v54, v52, v53
	v_cvt_pk_f16_f32 v53, v62, v63
	v_cvt_pk_f16_f32 v52, v60, v61
	v_mad_u64_u32 v[56:57], s[30:31], v115, s26, v[76:77]

.LBB3_74:
	s_or_b64 exec, exec, s[22:23]
	v_ashrrev_i32_e32 v64, 17, v119
.Lw3t78:
	s_cbranch_execz .Lw3c78
.Lw3b78:
	s_waitcnt vmcnt(4)
	v_mfma_f32_16x16x16_f16 v[56:59], v[72:73], v[48:49], v[60:63]
	v_cmp_ne_u32_e32 vcc, v64, v115
	s_cmp_lg_u64 vcc, 0
	s_cselect_b64 s[22:23], -1, 0
	v_mfma_f32_16x16x16_f16 v[48:51], v[72:73], v[50:51], v[52:55]
	s_and_b64 s[24:25], s[22:23], vcc
	s_and_saveexec_b64 s[22:23], s[24:25]
	s_cbranch_execz .LBB3_78
	v_cmp_gt_i32_e32 vcc, 16, v115
	s_and_saveexec_b64 s[24:25], vcc
	s_cbranch_execz .LBB3_77
	s_nop 1

.Lw3b79:
	v_cvt_pk_f16_f32 v51, v50, v51
	v_cvt_pk_f16_f32 v50, v48, v49
	v_cvt_pk_f16_f32 v49, v58, v59
	v_cvt_pk_f16_f32 v48, v56, v57
	v_mad_u64_u32 v[52:53], s[30:31], v115, s26, v[76:77]
	ds_write_b128 v52, v[48:51]
.LBB3_77:
	s_or_b64 exec, exec, s[24:25]
	s_nop 0
	v_mov_b32_e32 v48, 0
.Lw3t80:
	s_cbranch_execz .Lw3c80
.Lw3b80:
	v_mov_b32_e32 v115, v64
	v_mov_b32_e32 v49, v48
	v_mov_b32_e32 v50, v48
	v_mov_b32_e32 v51, v48
	v_mov_b32_e32 v56, v48
	v_mov_b32_e32 v57, v48
	v_mov_b32_e32 v58, v48
	v_mov_b32_e32 v59, v48
.LBB3_78:
	s_or_b64 exec, exec, s[22:23]
	v_ashrrev_i32_e32 v60, 17, v118
	s_waitcnt vmcnt(3)
	v_mfma_f32_16x16x16_f16 v[52:55], v[72:73], v[44:45], v[56:59]
	v_cmp_ne_u32_e32 vcc, v60, v115
	s_cmp_lg_u64 vcc, 0
	s_cselect_b64 s[22:23], -1, 0
.Lw3t81:
	s_cbranch_execz .Lw3c81

.LBB3_81:
	s_or_b64 exec, exec, s[24:25]
	s_nop 0
	v_mov_b32_e32 v44, 0
	v_mov_b32_e32 v115, v60
	v_mov_b32_e32 v45, v44
	v_mov_b32_e32 v46, v44
	v_mov_b32_e32 v47, v44
	v_mov_b32_e32 v52, v44
.Lw3t83:
	s_cbranch_execz .Lw3c83
.Lw3b83:
	v_mov_b32_e32 v53, v44
	v_mov_b32_e32 v54, v44
	v_mov_b32_e32 v55, v44
.LBB3_82:
	s_or_b64 exec, exec, s[22:23]
	v_ashrrev_i32_e32 v56, 17, v117
	s_waitcnt vmcnt(2)
	v_mfma_f32_16x16x16_f16 v[48:51], v[72:73], v[40:41], v[52:55]
	v_cmp_ne_u32_e32 vcc, v56, v115
	s_cmp_lg_u64 vcc, 0
	s_cselect_b64 s[22:23], -1, 0
	v_mfma_f32_16x16x16_f16 v[40:43], v[72:73], v[42:43], v[44:47]
	s_and_b64 s[24:25], s[22:23], vcc
	s_and_saveexec_b64 s[22:23], s[24:25]
.Lw3t84:
	s_cbranch_execz .Lw3c84
.Lw3b84:
	s_cbranch_execz .LBB3_86
	v_cmp_gt_i32_e32 vcc, 16, v115
	s_and_saveexec_b64 s[24:25], vcc
	s_cbranch_execz .LBB3_85
	s_nop 1
	v_cvt_pk_f16_f32 v43, v42, v43
	v_cvt_pk_f16_f32 v42, v40, v41
	v_cvt_pk_f16_f32 v41, v50, v51
	v_cvt_pk_f16_f32 v40, v48, v49
	v_mad_u64_u32 v[44:45], s[30:31], v115, s26, v[76:77]

.LBB3_86:
	s_or_b64 exec, exec, s[22:23]
	v_ashrrev_i32_e32 v52, 17, v116
.Lw3t86:
	s_cbranch_execz .Lw3c86
.Lw3b86:
	s_waitcnt vmcnt(1)
	v_mfma_f32_16x16x16_f16 v[44:47], v[72:73], v[36:37], v[48:51]
	v_cmp_ne_u32_e32 vcc, v52, v115
	s_cmp_lg_u64 vcc, 0
	s_cselect_b64 s[22:23], -1, 0
	v_mfma_f32_16x16x16_f16 v[36:39], v[72:73], v[38:39], v[40:43]
	s_and_b64 s[24:25], s[22:23], vcc
	s_and_saveexec_b64 s[22:23], s[24:25]
	s_cbranch_execz .LBB3_90
	v_cmp_gt_i32_e32 vcc, 16, v115
	s_and_saveexec_b64 s[24:25], vcc
	s_cbranch_execz .LBB3_89
	s_nop 1

.Lw3b87:
	v_cvt_pk_f16_f32 v39, v38, v39
	v_cvt_pk_f16_f32 v38, v36, v37
	v_cvt_pk_f16_f32 v37, v46, v47
	v_cvt_pk_f16_f32 v36, v44, v45
	v_mad_u64_u32 v[40:41], s[30:31], v115, s26, v[76:77]
	ds_write_b128 v40, v[36:39]
.LBB3_89:
	s_or_b64 exec, exec, s[24:25]
	s_nop 0
	v_mov_b32_e32 v36, 0
.Lw3t88:
	s_cbranch_execz .Lw3c88
.Lw3b88:
	v_mov_b32_e32 v115, v52
	v_mov_b32_e32 v37, v36
	v_mov_b32_e32 v38, v36
	v_mov_b32_e32 v39, v36
	v_mov_b32_e32 v44, v36
	v_mov_b32_e32 v45, v36
	v_mov_b32_e32 v46, v36
	v_mov_b32_e32 v47, v36
.LBB3_90:
	s_or_b64 exec, exec, s[22:23]
	s_waitcnt vmcnt(0)
	v_mfma_f32_16x16x16_f16 v[60:63], v[72:73], v[32:33], v[44:47]
	v_add_u32_e32 v32, 16, v113
	v_mfma_f32_16x16x16_f16 v[56:59], v[72:73], v[34:35], v[36:39]
.LBB3_91:
.Lw3t89:
	s_cbranch_execz .Lw3c89
.Lw3b89:
	v_mov_b32_e32 v113, v32
	v_mov_b32_e32 v116, v114
	s_branch .LBB3_22
.LBB3_92:
	v_cmp_gt_i32_e32 vcc, 16, v107
	s_and_saveexec_b64 s[20:21], vcc
	s_cbranch_execz .LBB3_17
	v_cvt_pk_f16_f32 v35, v111, v109
	v_cvt_pk_f16_f32 v34, v112, v110
	v_cvt_pk_f16_f32 v33, v106, v104
	v_cvt_pk_f16_f32 v32, v108, v105
	v_mad_u64_u32 v[36:37], s[22:23], v107, s26, v[76:77]
.Lw3t90:
	s_cbranch_execz .Lw3c90
.Lw3b90:
	ds_write_b128 v36, v[32:35]
	s_branch .LBB3_17
.LBB3_94:
	v_mov_b32_e32 v32, v28
	v_mov_b32_e32 v33, v24
	v_mov_b32_e32 v34, v29
	v_mov_b32_e32 v35, v25
	v_pk_add_f32 v[32:33], v[32:33], v[34:35]
	v_mov_b32_e32 v34, v30
	v_mov_b32_e32 v35, v26
	v_mov_b32_e32 v36, v31
	v_mov_b32_e32 v37, v27
	v_pk_add_f32 v[34:35], v[34:35], v[36:37]
.Lw3t91:
	s_cbranch_execz .Lw3c91
.Lw3b91:
	v_mov_b32_e32 v36, v20
	v_pk_add_f32 v[32:33], v[32:33], v[34:35]
	v_mov_b32_e32 v34, v21
	v_mov_b32_e32 v35, v22
	v_mov_b32_e32 v37, v23
	v_pk_add_f32 v[34:35], v[34:35], v[36:37]
	v_add_f32_e32 v32, 0, v32
	v_pk_add_f32 v[34:35], v[34:35], v[34:35] op_sel:[0,1] op_sel_hi:[1,0]
	v_add_f32_e32 v32, v32, v33
	v_add_f32_e32 v36, v16, v17
	v_add_f32_e32 v38, v18, v19

.Lw3b92:
	v_mov_b32_e32 v33, v12
	v_mov_b32_e32 v35, v13
	v_mov_b32_e32 v37, v14
	v_mov_b32_e32 v39, v15
	v_pk_add_f32 v[32:33], v[32:33], v[34:35]
	v_pk_add_f32 v[34:35], v[36:37], v[38:39]
	v_mov_b32_e32 v36, v8
	v_pk_add_f32 v[32:33], v[32:33], v[34:35]
	v_mov_b32_e32 v34, v9
	v_mov_b32_e32 v35, v10
	v_mov_b32_e32 v37, v11
	v_pk_add_f32 v[34:35], v[34:35], v[36:37]

.Lw3b93:
	v_pk_add_f32 v[32:33], v[32:33], v[32:33] op_sel:[0,1] op_sel_hi:[1,0]
	v_pk_add_f32 v[34:35], v[34:35], v[34:35] op_sel:[0,1] op_sel_hi:[1,0]
	v_add_f32_e32 v36, v4, v5
	v_add_f32_e32 v38, v6, v7
	v_mov_b32_e32 v33, v0
	v_mov_b32_e32 v35, v1
	v_mov_b32_e32 v37, v2
	v_mov_b32_e32 v39, v3
	v_pk_add_f32 v[32:33], v[32:33], v[34:35]
	v_pk_add_f32 v[34:35], v[36:37], v[38:39]

.Lw3b94:
	s_nop 0
	v_pk_add_f32 v[32:33], v[32:33], v[34:35]
	v_and_b32_e32 v34, 64, v100
	v_add_f32_e32 v32, v32, v33
	v_xor_b32_e32 v33, 16, v100
	v_add_u32_e32 v34, 64, v34
	v_cmp_lt_i32_e32 vcc, v33, v34
	s_nop 1
	v_cndmask_b32_e32 v33, v100, v33, vcc
	v_lshlrev_b32_e32 v40, 2, v33
	ds_bpermute_b32 v33, v40, v32
	s_waitcnt lgkmcnt(0)
	v_add_f32_e32 v32, v32, v33

.Lw3b95:
	v_xor_b32_e32 v33, 32, v100
	v_cmp_lt_i32_e32 vcc, v33, v34
	s_nop 1
	v_cndmask_b32_e32 v33, v100, v33, vcc
	v_lshlrev_b32_e32 v41, 2, v33
	ds_bpermute_b32 v33, v41, v32
	s_waitcnt lgkmcnt(0)
	v_add_f32_e32 v42, v32, v33
	v_fmamk_f32 v29, v42, 0xbc000000, v29
	v_fmamk_f32 v25, v42, 0xbc000000, v25
	v_fmamk_f32 v39, v42, 0xbc000000, v31

.Lw3b96:
	v_fmamk_f32 v38, v42, 0xbc000000, v30
	v_fmac_f32_e32 v28, 0xbc000000, v42
	v_fmamk_f32 v37, v42, 0xbc000000, v27
	v_fmac_f32_e32 v24, 0xbc000000, v42
	v_mov_b32_e32 v30, v29
	v_mov_b32_e32 v31, v25
	v_fmamk_f32 v36, v42, 0xbc000000, v26
	v_mov_b32_e32 v26, v28
	v_mov_b32_e32 v27, v24
	v_pk_mul_f32 v[30:31], v[30:31], v[30:31]

.Lw3b97:
	v_mov_b32_e32 v32, v39
	v_mov_b32_e32 v33, v37
	v_pk_fma_f32 v[26:27], v[26:27], v[26:27], v[30:31]
	v_mov_b32_e32 v30, v38
	v_mov_b32_e32 v31, v36
	v_pk_mul_f32 v[32:33], v[32:33], v[32:33]
	v_fmamk_f32 v35, v42, 0xbc000000, v21
	v_pk_fma_f32 v[30:31], v[30:31], v[30:31], v[32:33]
	v_fmamk_f32 v34, v42, 0xbc000000, v20

.Lw3b98:
	v_fmamk_f32 v23, v42, 0xbc000000, v23
	v_fmac_f32_e32 v22, 0xbc000000, v42
	v_pk_add_f32 v[26:27], v[26:27], v[30:31]
	v_pk_mul_f32 v[20:21], v[22:23], v[22:23]
	v_pk_mul_f32 v[30:31], v[34:35], v[34:35]
	v_fmamk_f32 v13, v42, 0xbc000000, v13
	v_pk_mov_b32 v[32:33], v[30:31], v[20:21] op_sel:[1,0]
	v_mov_b32_e32 v31, v21

.Lw3b99:
	v_pk_add_f32 v[20:21], v[32:33], v[30:31]
	v_fmac_f32_e32 v12, 0xbc000000, v42
	v_fmamk_f32 v33, v42, 0xbc000000, v19
	v_fmamk_f32 v32, v42, 0xbc000000, v18
	v_fmamk_f32 v19, v42, 0xbc000000, v15
	v_fmamk_f32 v18, v42, 0xbc000000, v14
	v_mul_f32_e32 v30, v12, v12
	v_mul_f32_e32 v31, v13, v13
	v_pk_add_f32 v[14:15], v[26:27], v[26:27] op_sel:[0,1] op_sel_hi:[1,0]

.Lw3b100:
	v_pk_add_f32 v[20:21], v[20:21], v[20:21] op_sel:[0,1] op_sel_hi:[1,0]
	v_fmamk_f32 v17, v42, 0xbc000000, v17
	v_mov_b32_e32 v15, v30
	v_mov_b32_e32 v21, v31
	v_fmac_f32_e32 v16, 0xbc000000, v42
	v_pk_add_f32 v[14:15], v[14:15], v[20:21]
	v_mul_f32_e32 v20, v17, v17
	v_mul_f32_e32 v26, v33, v33
	v_mul_f32_e32 v43, v18, v18
	v_mul_f32_e32 v44, v19, v19

.Lw3b101:
	v_pk_fma_f32 v[20:21], v[16:17], v[16:17], v[20:21] op_sel_hi:[1,1,0]
	v_pk_fma_f32 v[26:27], v[32:33], v[32:33], v[26:27] op_sel_hi:[1,1,0]
	v_mov_b32_e32 v21, v43
	v_mov_b32_e32 v27, v44
	v_pk_add_f32 v[20:21], v[20:21], v[26:27]
	v_fmamk_f32 v11, v42, 0xbc000000, v11
	v_pk_add_f32 v[14:15], v[14:15], v[20:21]
	v_fmamk_f32 v21, v42, 0xbc000000, v9
	v_fmamk_f32 v20, v42, 0xbc000000, v8

.Lw3b102:
	v_fmac_f32_e32 v10, 0xbc000000, v42
	v_pk_mul_f32 v[8:9], v[10:11], v[10:11]
	v_pk_mul_f32 v[26:27], v[20:21], v[20:21]
	v_fmamk_f32 v1, v42, 0xbc000000, v1
	v_pk_mov_b32 v[30:31], v[26:27], v[8:9] op_sel:[1,0]
	v_mov_b32_e32 v27, v9
	v_pk_add_f32 v[8:9], v[30:31], v[26:27]
	v_fmac_f32_e32 v0, 0xbc000000, v42

.Lw3b103:
	v_fmamk_f32 v27, v42, 0xbc000000, v7
	v_fmamk_f32 v26, v42, 0xbc000000, v6
	v_mul_f32_e32 v30, v0, v0
	v_mul_f32_e32 v31, v1, v1
	v_pk_add_f32 v[6:7], v[14:15], v[14:15] op_sel:[0,1] op_sel_hi:[1,0]
	v_pk_add_f32 v[8:9], v[8:9], v[8:9] op_sel:[0,1] op_sel_hi:[1,0]
	v_fmamk_f32 v5, v42, 0xbc000000, v5
	v_mov_b32_e32 v7, v30
	v_mov_b32_e32 v9, v31

.Lw3b104:
	v_fmac_f32_e32 v4, 0xbc000000, v42
	v_fmamk_f32 v3, v42, 0xbc000000, v3
	v_fmamk_f32 v2, v42, 0xbc000000, v2
	v_pk_add_f32 v[6:7], v[6:7], v[8:9]
	v_mul_f32_e32 v8, v5, v5
	v_mul_f32_e32 v14, v27, v27
	v_mul_f32_e32 v42, v2, v2
	v_mul_f32_e32 v43, v3, v3
	v_pk_fma_f32 v[8:9], v[4:5], v[4:5], v[8:9] op_sel_hi:[1,1,0]
	v_pk_fma_f32 v[14:15], v[26:27], v[26:27], v[14:15] op_sel_hi:[1,1,0]

.Lw3b105:
	v_mov_b32_e32 v9, v42
	v_mov_b32_e32 v15, v43
	v_pk_add_f32 v[8:9], v[8:9], v[14:15]
	s_nop 0
	v_pk_add_f32 v[6:7], v[6:7], v[8:9]
	s_nop 0
	v_add_f32_e32 v6, v6, v7
	ds_bpermute_b32 v7, v40, v6
	s_waitcnt lgkmcnt(0)
	v_add_f32_e32 v6, v6, v7
	ds_bpermute_b32 v7, v41, v6

.Lw3b106:
	s_waitcnt lgkmcnt(0)
	v_add_f32_e32 v6, v6, v7
	v_fmamk_f32 v6, v6, 0x3c000000, v98
	v_mul_f32_e32 v7, 0x4b800000, v6
	v_cmp_gt_f32_e32 vcc, s28, v6
	s_nop 1
	v_cndmask_b32_e32 v6, v6, v7, vcc
	v_rsq_f32_e32 v14, v6
	ds_read_b128 v[6:9], v96 offset:512
	ds_read_b128 v[40:43], v96 offset:528

.Lw3b107:
	ds_read_b128 v[44:47], v96 offset:1024
	ds_read_b128 v[48:51], v96 offset:1040
	v_mul_f32_e32 v15, 0x45800000, v14
	v_cndmask_b32_e32 v30, v14, v15, vcc
	v_pk_mul_f32 v[14:15], v[30:31], v[28:29] op_sel_hi:[0,1]
	s_waitcnt lgkmcnt(1)
	v_pk_fma_f32 v[6:7], v[6:7], v[14:15], v[44:45]
	v_pk_mul_f32 v[28:29], v[30:31], v[38:39] op_sel_hi:[0,1]
	v_pk_mul_f32 v[14:15], v[6:7], v[6:7]

.Lw3b108:
	v_pk_fma_f32 v[8:9], v[8:9], v[28:29], v[46:47]
	v_fmamk_f32 v14, v14, 0xbdd2d3e8, v99
	v_fmamk_f32 v15, v15, 0xbdd2d3e8, v99
	v_mul_f32_e32 v14, v6, v14
	v_mul_f32_e32 v15, v7, v15
	v_exp_f32_e32 v14, v14
	v_exp_f32_e32 v15, v15
	v_pk_mul_f32 v[28:29], v[8:9], v[8:9]
	v_add_f32_e32 v14, 1.0, v14
	v_add_f32_e32 v15, 1.0, v15

.Lw3b109:
	v_rcp_f32_e32 v14, v14
	v_rcp_f32_e32 v15, v15
	v_fmamk_f32 v28, v28, 0xbdd2d3e8, v99
	v_mul_f32_e32 v28, v8, v28
	v_exp_f32_e32 v28, v28
	v_pk_mul_f32 v[6:7], v[6:7], v[14:15]
	v_fmamk_f32 v14, v29, 0xbdd2d3e8, v99
	v_mul_f32_e32 v14, v9, v14
	v_exp_f32_e32 v29, v14
	v_pk_mul_f32 v[14:15], v[30:31], v[24:25] op_sel_hi:[0,1]
	s_waitcnt lgkmcnt(0)

.Lw3b110:
	v_pk_fma_f32 v[14:15], v[40:41], v[14:15], v[48:49]
	v_cvt_pk_f16_f32 v6, v6, v7
	v_pk_mul_f32 v[24:25], v[14:15], v[14:15]
	v_add_f32_e32 v7, 1.0, v28
	v_fmamk_f32 v24, v24, 0xbdd2d3e8, v99
	v_mul_f32_e32 v24, v14, v24
	v_exp_f32_e32 v24, v24
	v_rcp_f32_e32 v28, v7
	v_add_f32_e32 v7, 1.0, v29
	v_rcp_f32_e32 v29, v7
	v_add_f32_e32 v7, 1.0, v24

.Lw3b111:
	v_fmamk_f32 v24, v25, 0xbdd2d3e8, v99
	v_mul_f32_e32 v31, v15, v24
	v_pk_mul_f32 v[24:25], v[30:31], v[36:37] op_sel_hi:[0,1]
	v_pk_fma_f32 v[24:25], v[42:43], v[24:25], v[50:51]
	v_exp_f32_e32 v31, v31
	v_pk_mul_f32 v[36:37], v[24:25], v[24:25]
	v_rcp_f32_e32 v38, v7
	v_fmamk_f32 v36, v36, 0xbdd2d3e8, v99
	v_fmamk_f32 v37, v37, 0xbdd2d3e8, v99

.Lw3b112:
	v_mul_f32_e32 v36, v24, v36
	v_mul_f32_e32 v37, v25, v37
	v_exp_f32_e32 v36, v36
	v_exp_f32_e32 v37, v37
	v_add_f32_e32 v7, 1.0, v31
	v_mov_b32_e32 v31, v84
	v_add_f32_e32 v36, 1.0, v36
	v_add_f32_e32 v37, 1.0, v37
	v_rcp_f32_e32 v36, v36
	v_rcp_f32_e32 v37, v37
	v_rcp_f32_e32 v39, v7
	v_pk_mul_f32 v[8:9], v[8:9], v[28:29]
	v_pk_mul_f32 v[24:25], v[24:25], v[36:37]

.Lw3b113:
	s_nop 0
	s_nop 0
	v_lshl_add_u32 v7, v31, 2, v101
	v_add_u32_e32 v52, 0x420, v7
	v_add_u32_e32 v46, 0x428, v7
	v_add_u32_e32 v50, 0x430, v7
	ds_read2_b32 v[36:37], v7 offset0:138 offset1:139
	ds_read2_b32 v[40:41], v7 offset0:142 offset1:143
	ds_read2_b32 v[42:43], v7 offset0:140 offset1:141

.Lw3b114:
	ds_read2_b32 v[44:45], v7 offset0:136 offset1:137
	v_add_u32_e32 v7, 0x438, v7
	ds_read2_b32 v[46:47], v46 offset1:1
	ds_read2_b32 v[48:49], v7 offset1:1
	ds_read2_b32 v[50:51], v50 offset1:1
	ds_read2_b32 v[52:53], v52 offset1:1
	v_cvt_pk_f16_f32 v7, v8, v9

.Lw3b115:
	v_pk_mul_f32 v[8:9], v[14:15], v[38:39]
	s_nop 0
	v_cvt_pk_f16_f32 v8, v8, v9
	v_pk_mul_f32 v[14:15], v[30:31], v[34:35] op_sel_hi:[0,1]
	s_waitcnt lgkmcnt(0)
	v_pk_fma_f32 v[14:15], v[44:45], v[14:15], v[52:53]
	v_pk_mul_f32 v[22:23], v[30:31], v[22:23] op_sel_hi:[0,1]
	v_pk_mul_f32 v[28:29], v[14:15], v[14:15]
	v_pk_fma_f32 v[22:23], v[36:37], v[22:23], v[46:47]

.Lw3b116:
	v_fmamk_f32 v9, v28, 0xbdd2d3e8, v99
	v_mul_f32_e32 v9, v14, v9
	v_fmamk_f32 v28, v29, 0xbdd2d3e8, v99
	v_exp_f32_e32 v9, v9
	v_mul_f32_e32 v28, v15, v28
	v_exp_f32_e32 v29, v28
	v_pk_mul_f32 v[34:35], v[22:23], v[22:23]
	v_add_f32_e32 v9, 1.0, v9
	v_rcp_f32_e32 v28, v9
	v_add_f32_e32 v9, 1.0, v29
	v_rcp_f32_e32 v29, v9

.Lw3b117:
	v_fmamk_f32 v9, v34, 0xbdd2d3e8, v99
	v_mul_f32_e32 v9, v22, v9
	v_exp_f32_e32 v34, v9
	v_cvt_pk_f16_f32 v9, v24, v25
	v_fmamk_f32 v24, v35, 0xbdd2d3e8, v99
	v_pk_mul_f32 v[16:17], v[30:31], v[16:17] op_sel_hi:[0,1]
	v_mul_f32_e32 v24, v23, v24
	v_pk_fma_f32 v[16:17], v[42:43], v[16:17], v[50:51]
	v_pk_mul_f32 v[14:15], v[14:15], v[28:29]

.Lw3b118:
	v_exp_f32_e32 v29, v24
	v_pk_mul_f32 v[24:25], v[16:17], v[16:17]
	v_cvt_pk_f16_f32 v14, v14, v15
	v_fmamk_f32 v24, v24, 0xbdd2d3e8, v99
	v_mul_f32_e32 v24, v16, v24
	v_exp_f32_e32 v24, v24
	v_add_f32_e32 v15, 1.0, v34
	v_rcp_f32_e32 v28, v15
	v_add_f32_e32 v15, 1.0, v29
	v_rcp_f32_e32 v29, v15
	v_add_f32_e32 v15, 1.0, v24
	v_fmamk_f32 v24, v25, 0xbdd2d3e8, v99

.Lw3b119:
	v_mul_f32_e32 v34, v17, v24
	v_pk_mul_f32 v[24:25], v[30:31], v[32:33] op_sel_hi:[0,1]
	v_pk_fma_f32 v[24:25], v[40:41], v[24:25], v[48:49]
	v_exp_f32_e32 v35, v34
	v_pk_mul_f32 v[32:33], v[24:25], v[24:25]
	v_rcp_f32_e32 v34, v15
	v_fmamk_f32 v32, v32, 0xbdd2d3e8, v99
	v_fmamk_f32 v33, v33, 0xbdd2d3e8, v99
	v_mul_f32_e32 v32, v24, v32

.Lw3b120:
	v_mul_f32_e32 v33, v25, v33
	v_exp_f32_e32 v32, v32
	v_exp_f32_e32 v33, v33
	v_add_f32_e32 v15, 1.0, v35
	v_rcp_f32_e32 v35, v15
	v_add_f32_e32 v32, 1.0, v32
	v_add_f32_e32 v33, 1.0, v33
	v_rcp_f32_e32 v32, v32
	v_rcp_f32_e32 v33, v33
	v_pk_mul_f32 v[22:23], v[22:23], v[28:29]
	v_pk_mul_f32 v[16:17], v[16:17], v[34:35]
	v_pk_mul_f32 v[24:25], v[24:25], v[32:33]

.Lw3b121:
	s_nop 0
	v_cvt_pk_f16_f32 v16, v16, v17
	v_lshl_add_u32 v15, v31, 2, v101
	v_add_u32_e32 v48, 0x440, v15
	v_add_u32_e32 v42, 0x448, v15
	v_add_u32_e32 v46, 0x450, v15
	ds_read2_b32 v[32:33], v15 offset0:146 offset1:147
	ds_read2_b32 v[36:37], v15 offset0:150 offset1:151

.Lw3b122:
	ds_read2_b32 v[38:39], v15 offset0:148 offset1:149
	ds_read2_b32 v[40:41], v15 offset0:144 offset1:145
	v_add_u32_e32 v15, 0x458, v15
	ds_read2_b32 v[42:43], v42 offset1:1
	ds_read2_b32 v[44:45], v15 offset1:1
	ds_read2_b32 v[46:47], v46 offset1:1
	ds_read2_b32 v[48:49], v48 offset1:1
	v_cvt_pk_f16_f32 v15, v22, v23

.Lw3b123:
	v_pk_mul_f32 v[12:13], v[30:31], v[12:13] op_sel_hi:[0,1]
	s_waitcnt lgkmcnt(0)
	v_pk_fma_f32 v[12:13], v[40:41], v[12:13], v[48:49]
	v_pk_mul_f32 v[18:19], v[30:31], v[18:19] op_sel_hi:[0,1]
	v_pk_mul_f32 v[22:23], v[12:13], v[12:13]
	v_pk_fma_f32 v[28:29], v[32:33], v[18:19], v[42:43]
	v_fmamk_f32 v17, v22, 0xbdd2d3e8, v99
	v_mul_f32_e32 v17, v12, v17

.Lw3b124:
	v_fmamk_f32 v22, v23, 0xbdd2d3e8, v99
	v_exp_f32_e32 v17, v17
	v_mul_f32_e32 v22, v13, v22
	v_exp_f32_e32 v23, v22
	v_pk_mul_f32 v[18:19], v[28:29], v[28:29]
	v_add_f32_e32 v17, 1.0, v17
	v_rcp_f32_e32 v22, v17
	v_add_f32_e32 v17, 1.0, v23
	v_rcp_f32_e32 v23, v17
	v_fmamk_f32 v17, v18, 0xbdd2d3e8, v99
	v_pk_mul_f32 v[10:11], v[30:31], v[10:11] op_sel_hi:[0,1]

.Lw3b125:
	v_mul_f32_e32 v17, v28, v17
	v_pk_mul_f32 v[12:13], v[12:13], v[22:23]
	v_pk_fma_f32 v[10:11], v[36:37], v[10:11], v[44:45]
	v_cvt_pk_f16_f32 v18, v12, v13
	v_fmamk_f32 v12, v19, 0xbdd2d3e8, v99
	v_mul_f32_e32 v12, v29, v12
	v_exp_f32_e32 v19, v12
	v_pk_mul_f32 v[12:13], v[30:31], v[20:21] op_sel_hi:[0,1]
	v_pk_fma_f32 v[12:13], v[38:39], v[12:13], v[46:47]

.Lw3b126:
	v_exp_f32_e32 v32, v17
	v_pk_mul_f32 v[20:21], v[12:13], v[12:13]
	v_add_f32_e32 v19, 1.0, v19
	v_fmamk_f32 v20, v20, 0xbdd2d3e8, v99
	v_mul_f32_e32 v20, v12, v20
	v_exp_f32_e32 v20, v20
	v_rcp_f32_e32 v23, v19
	v_cvt_pk_f16_f32 v17, v24, v25
	v_add_f32_e32 v22, 1.0, v32
	v_add_f32_e32 v19, 1.0, v20
	v_fmamk_f32 v20, v21, 0xbdd2d3e8, v99

.Lw3b127:
	v_mul_f32_e32 v24, v13, v20
	v_pk_mul_f32 v[20:21], v[10:11], v[10:11]
	v_exp_f32_e32 v25, v24
	v_fmamk_f32 v20, v20, 0xbdd2d3e8, v99
	v_fmamk_f32 v21, v21, 0xbdd2d3e8, v99
	v_mul_f32_e32 v20, v10, v20
	v_mul_f32_e32 v21, v11, v21
	v_exp_f32_e32 v20, v20
	v_exp_f32_e32 v21, v21
	v_rcp_f32_e32 v24, v19
	v_add_f32_e32 v19, 1.0, v25
	v_add_f32_e32 v20, 1.0, v20

.Lw3b128:
	v_add_f32_e32 v21, 1.0, v21
	v_rcp_f32_e32 v20, v20
	v_rcp_f32_e32 v21, v21
	v_rcp_f32_e32 v25, v19
	v_rcp_f32_e32 v22, v22
	v_pk_mul_f32 v[10:11], v[10:11], v[20:21]
	s_nop 0
	v_pk_mul_f32 v[12:13], v[12:13], v[24:25]
	v_lshl_add_u32 v19, v31, 2, v101
	v_add_u32_e32 v21, 0x468, v19
	ds_read2_b32 v[32:33], v19 offset0:154 offset1:155

.Lw3b129:
	ds_read2_b32 v[34:35], v19 offset0:158 offset1:159
	ds_read2_b32 v[36:37], v19 offset0:156 offset1:157
	ds_read2_b32 v[38:39], v19 offset0:152 offset1:153
	v_add_u32_e32 v20, 0x460, v19
	v_add_u32_e32 v31, 0x470, v19
	v_add_u32_e32 v19, 0x478, v19
	ds_read2_b32 v[40:41], v21 offset1:1

.Lw3b130:
	ds_read2_b32 v[42:43], v19 offset1:1
	ds_read2_b32 v[44:45], v31 offset1:1
	ds_read2_b32 v[46:47], v20 offset1:1
	v_pk_mul_f32 v[20:21], v[28:29], v[22:23]
	s_nop 0
	v_cvt_pk_f16_f32 v19, v20, v21
	v_cvt_pk_f16_f32 v20, v12, v13
	v_pk_mul_f32 v[4:5], v[30:31], v[4:5] op_sel_hi:[0,1]

.Lw3b131:
	s_waitcnt lgkmcnt(0)
	v_pk_fma_f32 v[4:5], v[38:39], v[4:5], v[46:47]
	v_cvt_pk_f16_f32 v21, v10, v11
	v_pk_mul_f32 v[12:13], v[4:5], v[4:5]
	v_pk_mul_f32 v[10:11], v[30:31], v[26:27] op_sel_hi:[0,1]
	v_fmamk_f32 v12, v12, 0xbdd2d3e8, v99
	v_fmamk_f32 v13, v13, 0xbdd2d3e8, v99
	v_mul_f32_e32 v12, v4, v12
	v_mul_f32_e32 v13, v5, v13

.Lw3b132:
	v_exp_f32_e32 v12, v12
	v_exp_f32_e32 v13, v13
	v_pk_fma_f32 v[10:11], v[32:33], v[10:11], v[40:41]
	v_pk_mul_f32 v[0:1], v[30:31], v[0:1] op_sel_hi:[0,1]
	v_add_f32_e32 v12, 1.0, v12
	v_add_f32_e32 v13, 1.0, v13
	v_rcp_f32_e32 v12, v12
	v_rcp_f32_e32 v13, v13
	v_pk_fma_f32 v[0:1], v[36:37], v[0:1], v[44:45]
	v_pk_mul_f32 v[2:3], v[30:31], v[2:3] op_sel_hi:[0,1]
	v_pk_fma_f32 v[2:3], v[34:35], v[2:3], v[42:43]

.Lw3b133:
	v_pk_mul_f32 v[4:5], v[4:5], v[12:13]
	v_pk_mul_f32 v[12:13], v[10:11], v[10:11]
	v_cvt_pk_f16_f32 v24, v4, v5
	v_fmamk_f32 v12, v12, 0xbdd2d3e8, v99
	v_fmamk_f32 v13, v13, 0xbdd2d3e8, v99
	v_mul_f32_e32 v12, v10, v12
	v_mul_f32_e32 v13, v11, v13
	v_exp_f32_e32 v12, v12
	v_exp_f32_e32 v13, v13

.Lw3b134:
	v_add_f32_e32 v4, 1.0, v12
	v_add_f32_e32 v5, 1.0, v13
	v_pk_mul_f32 v[12:13], v[0:1], v[0:1]
	v_rcp_f32_e32 v4, v4
	v_fmamk_f32 v12, v12, 0xbdd2d3e8, v99
	v_fmamk_f32 v13, v13, 0xbdd2d3e8, v99
	v_mul_f32_e32 v12, v0, v12
	v_mul_f32_e32 v13, v1, v13
	v_rcp_f32_e32 v5, v5
	v_exp_f32_e32 v12, v12
	v_exp_f32_e32 v13, v13
	v_pk_mul_f32 v[4:5], v[10:11], v[4:5]

.Lw3b135:
	v_add_f32_e32 v10, 1.0, v12
	v_add_f32_e32 v11, 1.0, v13
	v_pk_mul_f32 v[12:13], v[2:3], v[2:3]
	v_rcp_f32_e32 v10, v10
	v_fmamk_f32 v12, v12, 0xbdd2d3e8, v99
	v_fmamk_f32 v13, v13, 0xbdd2d3e8, v99
	v_mul_f32_e32 v12, v2, v12
	v_mul_f32_e32 v13, v3, v13
	v_exp_f32_e32 v12, v12
	v_exp_f32_e32 v13, v13
	v_rcp_f32_e32 v11, v11

.Lw3b136:
	v_cvt_pk_f16_f32 v25, v4, v5
	v_add_f32_e32 v12, 1.0, v12
	v_add_f32_e32 v13, 1.0, v13
	v_rcp_f32_e32 v12, v12
	v_rcp_f32_e32 v13, v13
	v_pk_mul_f32 v[0:1], v[0:1], v[10:11]
	s_nop 0
	v_cvt_pk_f16_f32 v26, v0, v1
	v_pk_mul_f32 v[0:1], v[2:3], v[12:13]
	s_nop 0
	v_cvt_pk_f16_f32 v27, v0, v1

.Lw3b137:
	ds_read_b128 v[0:3], v96 offset:1536
	ds_read_b128 v[10:13], v96 offset:1552
	ds_read_b128 v[30:33], v96 offset:1568
	ds_read_b128 v[34:37], v96 offset:1584
	ds_read_b128 v[38:41], v96 offset:1600
	ds_read_b128 v[42:45], v96 offset:1616
	ds_read_b128 v[46:49], v96 offset:1632

.Lw3b138:
	ds_read_b128 v[50:53], v96 offset:1648
	v_mov_b32_e32 v4, v77
	s_nop 0
	v_lshl_add_u32 v28, v4, 4, v102
	ds_read_b128 v[54:57], v28
	ds_read_b128 v[58:61], v28 offset:1024
	ds_read_b128 v[62:65], v28 offset:2048
	ds_read_b128 v[66:69], v28 offset:3072
	ds_read_b128 v[104:107], v28 offset:4096

.Lw3b139:
	ds_read_b128 v[108:111], v28 offset:5120
	ds_read_b128 v[112:115], v28 offset:6144
	ds_read_b128 v[116:119], v28 offset:7168
	s_waitcnt lgkmcnt(7)
	v_mfma_f32_16x16x32_f16 v[0:3], v[54:57], v[6:9], v[0:3]
	s_waitcnt lgkmcnt(6)
	v_mfma_f32_16x16x32_f16 v[10:13], v[58:61], v[6:9], v[10:13]
	s_waitcnt lgkmcnt(5)
	v_mfma_f32_16x16x32_f16 v[30:33], v[62:65], v[6:9], v[30:33]

.Lw3b140:
	s_waitcnt lgkmcnt(4)
	v_mfma_f32_16x16x32_f16 v[34:37], v[66:69], v[6:9], v[34:37]
	ds_read_b128 v[54:57], v28 offset:8192
	ds_read_b128 v[58:61], v28 offset:9216
	ds_read_b128 v[62:65], v28 offset:10240
	ds_read_b128 v[66:69], v28 offset:11264
	s_waitcnt lgkmcnt(7)
	v_mfma_f32_16x16x32_f16 v[38:41], v[104:107], v[6:9], v[38:41]

.Lw3b141:
	s_waitcnt lgkmcnt(6)
	v_mfma_f32_16x16x32_f16 v[42:45], v[108:111], v[6:9], v[42:45]
	s_waitcnt lgkmcnt(5)
	v_mfma_f32_16x16x32_f16 v[46:49], v[112:115], v[6:9], v[46:49]
	s_waitcnt lgkmcnt(4)
	v_mfma_f32_16x16x32_f16 v[4:7], v[116:119], v[6:9], v[50:53]
	s_nop 2
	ds_read_b128 v[50:53], v28 offset:12288
	ds_read_b128 v[104:107], v28 offset:13312
	ds_read_b128 v[108:111], v28 offset:14336

.Lw3b142:
	ds_read_b128 v[112:115], v28 offset:15360
	s_waitcnt lgkmcnt(7)
	v_mfma_f32_16x16x32_f16 v[0:3], v[54:57], v[14:17], v[0:3]
	s_waitcnt lgkmcnt(6)
	v_mfma_f32_16x16x32_f16 v[8:11], v[58:61], v[14:17], v[10:13]
	s_waitcnt lgkmcnt(5)
	v_mfma_f32_16x16x32_f16 v[30:33], v[62:65], v[14:17], v[30:33]
	s_waitcnt lgkmcnt(4)
	v_mfma_f32_16x16x32_f16 v[34:37], v[66:69], v[14:17], v[34:37]

.Lw3b143:
	ds_read_b128 v[54:57], v28 offset:16384
	ds_read_b128 v[58:61], v28 offset:17408
	ds_read_b128 v[62:65], v28 offset:18432
	ds_read_b128 v[66:69], v28 offset:19456
	s_waitcnt lgkmcnt(7)
	v_mfma_f32_16x16x32_f16 v[38:41], v[50:53], v[14:17], v[38:41]
	s_waitcnt lgkmcnt(6)
	v_mfma_f32_16x16x32_f16 v[42:45], v[104:107], v[14:17], v[42:45]
	s_waitcnt lgkmcnt(5)

.Lw3b144:
	v_mfma_f32_16x16x32_f16 v[46:49], v[108:111], v[14:17], v[46:49]
	s_waitcnt lgkmcnt(4)
	v_mfma_f32_16x16x32_f16 v[4:7], v[112:115], v[14:17], v[4:7]
	ds_read_b128 v[12:15], v28 offset:20480
	ds_read_b128 v[50:53], v28 offset:21504
	ds_read_b128 v[104:107], v28 offset:22528
	ds_read_b128 v[108:111], v28 offset:23552
	s_waitcnt lgkmcnt(7)
	v_mfma_f32_16x16x32_f16 v[0:3], v[54:57], v[18:21], v[0:3]

.Lw3b145:
	s_waitcnt lgkmcnt(6)
	v_mfma_f32_16x16x32_f16 v[8:11], v[58:61], v[18:21], v[8:11]
	s_waitcnt lgkmcnt(5)
	v_mfma_f32_16x16x32_f16 v[30:33], v[62:65], v[18:21], v[30:33]
	s_waitcnt lgkmcnt(4)
	v_mfma_f32_16x16x32_f16 v[34:37], v[66:69], v[18:21], v[34:37]
	ds_read_b128 v[54:57], v28 offset:24576
	ds_read_b128 v[58:61], v28 offset:25600
	ds_read_b128 v[62:65], v28 offset:26624

.Lw3b146:
	ds_read_b128 v[66:69], v28 offset:27648
	s_waitcnt lgkmcnt(7)
	v_mfma_f32_16x16x32_f16 v[12:15], v[12:15], v[18:21], v[38:41]
	s_waitcnt lgkmcnt(6)
	v_mfma_f32_16x16x32_f16 v[38:41], v[50:53], v[18:21], v[42:45]
	s_waitcnt lgkmcnt(5)
	v_mfma_f32_16x16x32_f16 v[42:45], v[104:107], v[18:21], v[46:49]
	s_waitcnt lgkmcnt(4)
	v_mfma_f32_16x16x32_f16 v[46:49], v[108:111], v[18:21], v[4:7]

.Lw3b147:
	s_nop 2
	ds_read_b128 v[4:7], v28 offset:28672
	ds_read_b128 v[50:53], v28 offset:29696
	ds_read_b128 v[104:107], v28 offset:30720
	ds_read_b128 v[108:111], v28 offset:31744
	s_waitcnt lgkmcnt(7)
	v_mfma_f32_16x16x32_f16 v[54:57], v[54:57], v[24:27], v[0:3]
	s_waitcnt lgkmcnt(6)
	v_mfma_f32_16x16x32_f16 v[58:61], v[58:61], v[24:27], v[8:11]

.Lw3b148:
	s_waitcnt lgkmcnt(5)
	v_mfma_f32_16x16x32_f16 v[20:23], v[62:65], v[24:27], v[30:33]
	s_waitcnt lgkmcnt(4)
	v_mfma_f32_16x16x32_f16 v[16:19], v[66:69], v[24:27], v[34:37]
	s_waitcnt lgkmcnt(0)
	v_mfma_f32_16x16x32_f16 v[0:3], v[108:111], v[24:27], v[46:49]
	v_mfma_f32_16x16x32_f16 v[12:15], v[4:7], v[24:27], v[12:15]
	v_mfma_f32_16x16x32_f16 v[8:11], v[50:53], v[24:27], v[38:41]
	v_mfma_f32_16x16x32_f16 v[4:7], v[104:107], v[24:27], v[42:45]

.Lw3b149:
	v_mul_f32_e32 v24, v54, v54
	v_fmamk_f32 v24, v24, 0xbdd2d3e8, v99
	v_mul_f32_e32 v24, v54, v24
	v_exp_f32_e32 v24, v24
	v_mul_f32_e32 v25, v55, v55
	v_mul_f32_e32 v26, v56, v56
	v_fmamk_f32 v25, v25, 0xbdd2d3e8, v99
	v_fmamk_f32 v26, v26, 0xbdd2d3e8, v99
	v_mul_f32_e32 v25, v55, v25
	v_add_f32_e32 v24, 1.0, v24
	v_mul_f32_e32 v26, v56, v26
	v_rcp_f32_e32 v24, v24

.Lw3b150:
	v_exp_f32_e32 v25, v25
	v_exp_f32_e32 v26, v26
	v_mul_f32_e32 v30, v57, v57
	v_mul_f32_e32 v31, v58, v58
	v_fmamk_f32 v30, v30, 0xbdd2d3e8, v99
	v_fmamk_f32 v31, v31, 0xbdd2d3e8, v99
	v_fma_mixlo_f16 v29, v54, v24, 0
	v_add_f32_e32 v24, 1.0, v25
	v_add_f32_e32 v25, 1.0, v26
	v_mul_f32_e32 v30, v57, v30
	v_mul_f32_e32 v31, v58, v31
	v_rcp_f32_e32 v24, v24

.Lw3b151:
	v_rcp_f32_e32 v25, v25
	v_exp_f32_e32 v30, v30
	v_exp_f32_e32 v31, v31
	v_mov_b32_e32 v26, v55
	v_mov_b32_e32 v27, v56
	v_pk_mul_f32 v[24:25], v[26:27], v[24:25]
	v_add_f32_e32 v26, 1.0, v30
	v_add_f32_e32 v27, 1.0, v31
	v_rcp_f32_e32 v26, v26
	v_rcp_f32_e32 v27, v27
	v_cvt_pk_f16_f32 v25, v24, v25
	v_pk_mov_b32 v[30:31], v[56:57], v[58:59] op_sel:[1,0]

.Lw3b152:
	v_pack_b32_f16 v24, v29, v25
	v_pk_mul_f32 v[26:27], v[30:31], v[26:27]
	v_mul_f32_e32 v29, v59, v59
	v_mul_f32_e32 v30, v60, v60
	v_fmamk_f32 v29, v29, 0xbdd2d3e8, v99
	v_fmamk_f32 v30, v30, 0xbdd2d3e8, v99
	v_mul_f32_e32 v29, v59, v29
	v_mul_f32_e32 v30, v60, v30
	v_exp_f32_e32 v29, v29
	v_exp_f32_e32 v30, v30
	v_cvt_pk_f16_f32 v32, v26, v27

.Lw3b153:
	v_mov_b32_e32 v31, v60
	v_add_f32_e32 v26, 1.0, v29
	v_add_f32_e32 v27, 1.0, v30
	v_rcp_f32_e32 v26, v26
	v_rcp_f32_e32 v27, v27
	v_mov_b32_e32 v30, v59
	v_alignbit_b32 v25, v32, v25, 16
	v_mul_f32_e32 v34, v20, v20
	v_pk_mul_f32 v[26:27], v[30:31], v[26:27]
	v_fmamk_f32 v34, v34, 0xbdd2d3e8, v99
	v_cvt_pk_f16_f32 v27, v26, v27

.Lw3b154:
	v_mul_f32_e32 v26, v61, v61
	v_fmamk_f32 v26, v26, 0xbdd2d3e8, v99
	v_mul_f32_e32 v26, v61, v26
	v_exp_f32_e32 v29, v26
	v_alignbit_b32 v26, v27, v32, 16
	ds_read_b128 v[30:33], v28 offset:32768
	v_mul_f32_e32 v34, v20, v34
	v_add_f32_e32 v29, 1.0, v29
	v_rcp_f32_e32 v29, v29
	v_lshrrev_b32_e32 v27, 16, v27
	v_exp_f32_e32 v38, v34

.Lw3b155:
	ds_read_b128 v[34:37], v28 offset:33792
	v_fma_mixhi_f16 v27, v61, v29, 0
	v_add_f32_e32 v29, 1.0, v38
	s_waitcnt lgkmcnt(1)
	v_mfma_f32_16x16x32_f16 v[24:27], v[30:33], v[24:27], 0
	v_mul_f32_e32 v30, v21, v21
	v_fmamk_f32 v30, v30, 0xbdd2d3e8, v99
	v_mul_f32_e32 v31, v22, v22
	v_mul_f32_e32 v30, v21, v30
	v_fmamk_f32 v31, v31, 0xbdd2d3e8, v99

.Lw3b156:
	v_rcp_f32_e32 v29, v29
	v_exp_f32_e32 v30, v30
	v_mul_f32_e32 v31, v22, v31
	v_exp_f32_e32 v31, v31
	v_fma_mixlo_f16 v29, v20, v29, 0
	v_add_f32_e32 v20, 1.0, v30
	v_rcp_f32_e32 v30, v20
	v_add_f32_e32 v20, 1.0, v31
	v_rcp_f32_e32 v31, v20
	v_mov_b32_e32 v20, v21
	v_mov_b32_e32 v21, v22
	v_mul_f32_e32 v22, v23, v23
	v_fmamk_f32 v22, v22, 0xbdd2d3e8, v99

.Lw3b157:
	v_mul_f32_e32 v32, v16, v16
	v_mul_f32_e32 v22, v23, v22
	v_fmamk_f32 v32, v32, 0xbdd2d3e8, v99
	v_exp_f32_e32 v22, v22
	v_mul_f32_e32 v32, v16, v32
	v_exp_f32_e32 v32, v32
	v_pk_mul_f32 v[20:21], v[20:21], v[30:31]
	v_add_f32_e32 v22, 1.0, v22
	v_rcp_f32_e32 v30, v22
	v_add_f32_e32 v22, 1.0, v32
	v_rcp_f32_e32 v31, v22
	v_pk_mov_b32 v[22:23], v[22:23], v[16:17] op_sel:[1,0]

.Lw3b158:
	v_cvt_pk_f16_f32 v21, v20, v21
	v_mul_f32_e32 v16, v17, v17
	v_pk_mul_f32 v[22:23], v[22:23], v[30:31]
	v_pack_b32_f16 v20, v29, v21
	v_cvt_pk_f16_f32 v29, v22, v23
	v_fmamk_f32 v16, v16, 0xbdd2d3e8, v99
	v_mul_f32_e32 v22, v18, v18
	v_mul_f32_e32 v16, v17, v16
	v_fmamk_f32 v22, v22, 0xbdd2d3e8, v99

.Lw3b159:
	v_exp_f32_e32 v16, v16
	v_mul_f32_e32 v22, v18, v22
	v_exp_f32_e32 v23, v22
	v_alignbit_b32 v21, v29, v21, 16
	v_add_f32_e32 v16, 1.0, v16
	v_rcp_f32_e32 v22, v16
	v_add_f32_e32 v16, 1.0, v23
	v_rcp_f32_e32 v23, v16
	v_mul_f32_e32 v16, v19, v19
	v_fmamk_f32 v16, v16, 0xbdd2d3e8, v99
	v_mul_f32_e32 v16, v19, v16
	v_exp_f32_e32 v30, v16
	v_mov_b32_e32 v16, v17

.Lw3b160:
	v_mov_b32_e32 v17, v18
	v_pk_mul_f32 v[16:17], v[16:17], v[22:23]
	v_add_f32_e32 v18, 1.0, v30
	v_rcp_f32_e32 v18, v18
	v_cvt_pk_f16_f32 v16, v16, v17
	v_lshrrev_b32_e32 v23, 16, v16
	v_alignbit_b32 v22, v16, v29, 16
	v_fma_mixhi_f16 v23, v19, v18, 0
	s_waitcnt lgkmcnt(0)
	s_nop 0
	v_mfma_f32_16x16x32_f16 v[16:19], v[34:37], v[20:23], v[24:27]

.Lw3b161:
	v_mul_f32_e32 v20, v12, v12
	v_fmamk_f32 v20, v20, 0xbdd2d3e8, v99
	v_mul_f32_e32 v20, v12, v20
	v_exp_f32_e32 v20, v20
	v_mul_f32_e32 v21, v13, v13
	v_fmamk_f32 v21, v21, 0xbdd2d3e8, v99
	v_mul_f32_e32 v22, v14, v14
	v_mul_f32_e32 v21, v13, v21
	v_add_f32_e32 v20, 1.0, v20
	v_fmamk_f32 v22, v22, 0xbdd2d3e8, v99
	v_rcp_f32_e32 v20, v20

.Lw3b162:
	v_exp_f32_e32 v21, v21
	v_mul_f32_e32 v22, v14, v22
	v_exp_f32_e32 v22, v22
	v_fma_mixlo_f16 v23, v12, v20, 0
	v_add_f32_e32 v12, 1.0, v21
	v_rcp_f32_e32 v20, v12
	v_add_f32_e32 v12, 1.0, v22
	v_rcp_f32_e32 v21, v12
	v_mov_b32_e32 v12, v13
	v_mov_b32_e32 v13, v14
	v_mul_f32_e32 v14, v15, v15
	v_fmamk_f32 v14, v14, 0xbdd2d3e8, v99
	v_mul_f32_e32 v22, v8, v8

.Lw3b163:
	v_mul_f32_e32 v14, v15, v14
	v_fmamk_f32 v22, v22, 0xbdd2d3e8, v99
	v_exp_f32_e32 v14, v14
	v_mul_f32_e32 v22, v8, v22
	v_exp_f32_e32 v22, v22
	v_pk_mul_f32 v[12:13], v[12:13], v[20:21]
	v_add_f32_e32 v14, 1.0, v14
	v_rcp_f32_e32 v20, v14
	v_add_f32_e32 v14, 1.0, v22
	v_rcp_f32_e32 v21, v14
	v_pk_mov_b32 v[14:15], v[14:15], v[8:9] op_sel:[1,0]
	v_mul_f32_e32 v8, v9, v9

.Lw3b164:
	v_fmamk_f32 v8, v8, 0xbdd2d3e8, v99
	v_pk_mul_f32 v[14:15], v[14:15], v[20:21]
	v_mul_f32_e32 v20, v10, v10
	v_mul_f32_e32 v8, v9, v8
	v_fmamk_f32 v20, v20, 0xbdd2d3e8, v99
	v_exp_f32_e32 v8, v8
	v_mul_f32_e32 v20, v10, v20
	v_exp_f32_e32 v20, v20
	v_cvt_pk_f16_f32 v21, v14, v15
	v_add_f32_e32 v8, 1.0, v8
	v_rcp_f32_e32 v14, v8

.Lw3b165:
	v_add_f32_e32 v8, 1.0, v20
	v_rcp_f32_e32 v15, v8
	v_mov_b32_e32 v8, v9
	v_mov_b32_e32 v9, v10
	v_cvt_pk_f16_f32 v13, v12, v13
	v_pk_mul_f32 v[8:9], v[8:9], v[14:15]
	v_pack_b32_f16 v12, v23, v13
	v_cvt_pk_f16_f32 v8, v8, v9
	v_mul_f32_e32 v9, v11, v11
	v_fmamk_f32 v9, v9, 0xbdd2d3e8, v99

.Lw3b166:
	v_mul_f32_e32 v9, v11, v9
	v_exp_f32_e32 v9, v9
	v_alignbit_b32 v13, v21, v13, 16
	v_alignbit_b32 v14, v8, v21, 16
	ds_read_b128 v[20:23], v28 offset:34816
	v_lshrrev_b32_e32 v15, 16, v8
	v_add_f32_e32 v8, 1.0, v9
	v_rcp_f32_e32 v8, v8
	v_mul_f32_e32 v9, v4, v4
	v_fmamk_f32 v9, v9, 0xbdd2d3e8, v99
	v_mul_f32_e32 v9, v4, v9

.Lw3b167:
	v_exp_f32_e32 v24, v9
	v_fma_mixhi_f16 v15, v11, v8, 0
	ds_read_b128 v[8:11], v28 offset:35840
	s_waitcnt lgkmcnt(1)
	v_mfma_f32_16x16x32_f16 v[12:15], v[20:23], v[12:15], v[16:19]
	s_nop 2
	v_mul_f32_e32 v17, v5, v5
	v_fmamk_f32 v17, v17, 0xbdd2d3e8, v99
	v_mul_f32_e32 v18, v6, v6
	v_add_f32_e32 v16, 1.0, v24
	v_mul_f32_e32 v17, v5, v17

.Lw3b168:
	v_fmamk_f32 v18, v18, 0xbdd2d3e8, v99
	v_rcp_f32_e32 v16, v16
	v_exp_f32_e32 v17, v17
	v_mul_f32_e32 v18, v6, v18
	v_exp_f32_e32 v18, v18
	v_fma_mixlo_f16 v19, v4, v16, 0
	v_add_f32_e32 v4, 1.0, v17
	v_rcp_f32_e32 v16, v4
	v_add_f32_e32 v4, 1.0, v18
	v_rcp_f32_e32 v17, v4
	v_mov_b32_e32 v4, v5
	v_mov_b32_e32 v5, v6
	v_mul_f32_e32 v6, v7, v7

.Lw3b169:
	v_fmamk_f32 v6, v6, 0xbdd2d3e8, v99
	v_mul_f32_e32 v18, v0, v0
	v_mul_f32_e32 v6, v7, v6
	v_fmamk_f32 v18, v18, 0xbdd2d3e8, v99
	v_exp_f32_e32 v6, v6
	v_mul_f32_e32 v18, v0, v18
	v_exp_f32_e32 v18, v18
	v_pk_mul_f32 v[4:5], v[4:5], v[16:17]
	v_add_f32_e32 v6, 1.0, v6
	v_rcp_f32_e32 v16, v6
	v_add_f32_e32 v6, 1.0, v18
	v_rcp_f32_e32 v17, v6

.Lw3b170:
	v_pk_mov_b32 v[6:7], v[6:7], v[0:1] op_sel:[1,0]
	v_mul_f32_e32 v0, v1, v1
	v_fmamk_f32 v0, v0, 0xbdd2d3e8, v99
	v_pk_mul_f32 v[6:7], v[6:7], v[16:17]
	v_mul_f32_e32 v0, v1, v0
	v_cvt_pk_f16_f32 v16, v6, v7
	v_mul_f32_e32 v6, v2, v2
	v_fmamk_f32 v6, v6, 0xbdd2d3e8, v99
	v_exp_f32_e32 v0, v0
	v_mul_f32_e32 v6, v2, v6

.Lw3b171:
	v_exp_f32_e32 v7, v6
	v_cvt_pk_f16_f32 v5, v4, v5
	v_add_f32_e32 v0, 1.0, v0
	v_rcp_f32_e32 v6, v0
	v_add_f32_e32 v0, 1.0, v7
	v_rcp_f32_e32 v7, v0
	v_mul_f32_e32 v0, v3, v3
	v_fmamk_f32 v0, v0, 0xbdd2d3e8, v99
	v_mul_f32_e32 v0, v3, v0
	v_exp_f32_e32 v17, v0
	v_mov_b32_e32 v0, v1
	v_mov_b32_e32 v1, v2
	v_pk_mul_f32 v[0:1], v[0:1], v[6:7]

.Lw3b172:
	v_add_f32_e32 v2, 1.0, v17
	v_rcp_f32_e32 v2, v2
	v_cvt_pk_f16_f32 v0, v0, v1
	v_lshrrev_b32_e32 v7, 16, v0
	v_pack_b32_f16 v4, v19, v5
	v_alignbit_b32 v5, v16, v5, 16
	v_alignbit_b32 v6, v0, v16, 16
	v_fma_mixhi_f16 v7, v3, v2, 0
	s_waitcnt lgkmcnt(0)

.Lw3b173:
	s_nop 0
	v_mfma_f32_16x16x32_f16 v[0:3], v[8:11], v[4:7], v[12:15]
	s_and_saveexec_b64 s[14:15], s[4:5]
	s_xor_b64 s[14:15], exec, s[14:15]
	s_cbranch_execz .LBB3_9
	s_load_dwordx2 s[20:21], s[16:17], 0x0
	s_nop 3
	v_or_b32_e32 v2, s10, v80
	v_ashrrev_i32_e32 v3, 31, v2
	v_lshl_add_u64 v[2:3], v[2:3], 3, s[6:7]
	s_waitcnt lgkmcnt(0)
	v_pk_add_f32 v[0:1], v[0:1], s[20:21]

.Lw3b174:
	global_store_dwordx2 v[2:3], v[0:1], off
	s_branch .LBB3_9
